# retention-gate epilogue: ten of the twelve second-half loads prefetched during first-half compute into dead registers (copies at the old site)
# speedup vs baseline: 1.0011x; 1.0011x over previous
;     __device__ __forceinline__ void operator()(const f32x4 (&acc)[2][2][4][2], const Unit& u, int wr, int wc, int fr, int fq) const {
;         const int row0 = u.pm * BM + wr * 64 + fr, col0 = u.pn * HALF + wc * 32 + 8 * fq, head = u.pn >> 2;
; #pragma unroll
;         for (int ai = 0; ai < 2; ++ai) {
;             f32x4 stv[4]; u32x4 yfv[4], ybv[4];
; #pragma unroll
;             for (int m = 0; m < 4; ++m) { const int row = row0 + ai * HALF + m * 16;
;                 stv[m] = *(const f32x4*)(ST + (size_t)row * 16 + head * 4); yfv[m] = *(const u32x4*)(Y + (size_t)row * 2048 + col0); ybv[m] = *(const u32x4*)(YB + (size_t)row * 2048 + col0); }
; #pragma unroll
;             for (int m = 0; m < 4; ++m) { const int row = row0 + ai * HALF + m * 16; const float r = tab[u.idx * 256 + (row & 255)];
;                 const f32x4 st = stv[m];
;                 const float muf = __builtin_amdgcn_ldexpf(st[0], -9), mub = __builtin_amdgcn_ldexpf(st[2], -9); float eps = 1e-6f; asm volatile("" : "+s"(eps));
;                 const float rf = __builtin_amdgcn_rsqf(fmaxf(__builtin_amdgcn_ldexpf(st[1], -9) - muf * muf, 0.f) + eps), rb = __builtin_amdgcn_rsqf(fmaxf(__builtin_amdgcn_ldexpf(st[3], -9) - mub * mub, 0.f) + eps);
;                 const float cf = rf * r, cb = rb * r, df = -muf * cf, db = -mub * cb, kr = -1.4426950409f * r;
.LBB0_346:
	s_and_b32 s36, s33, -4
	s_ashr_i32 s37, s36, 31
	v_lshl_add_u32 v190, s44, 8, v217
	v_lshl_or_b32 v108, s33, 7, v223
	s_lshl_b64 s[36:37], s[36:37], 2
	v_ashrrev_i32_e32 v109, 31, v108
	s_add_u32 s44, s74, s36
	v_ashrrev_i32_e32 v191, 31, v190
	s_addc_u32 s45, s75, s37
	v_lshlrev_b64 v[188:189], 1, v[108:109]
	v_lshlrev_b64 v[108:109], 6, v[190:191]
	v_lshl_add_u64 v[108:109], s[44:45], 0, v[108:109]
	global_load_dwordx4 v[200:203], v[108:109], off
	v_readlane_b32 s16, v254, 5
	v_lshl_add_u64 v[192:193], s[4:5], 0, v[188:189]
	v_readlane_b32 s22, v254, 11
	v_readlane_b32 s23, v254, 12
	v_lshlrev_b64 v[214:215], 12, v[190:191]
	v_lshl_add_u64 v[108:109], v[192:193], 0, v[214:215]
	v_lshl_add_u64 v[194:195], s[22:23], 0, v[188:189]
	global_load_dwordx4 v[168:171], v[108:109], off
	v_lshl_add_u64 v[108:109], v[194:195], 0, v[214:215]
	global_load_dwordx4 v[172:175], v[108:109], off
	v_or_b32_e32 v108, 16, v190
	v_ashrrev_i32_e32 v109, 31, v108
	v_lshlrev_b64 v[110:111], 6, v[108:109]
	v_lshl_add_u64 v[110:111], s[44:45], 0, v[110:111]
	global_load_dwordx4 v[164:167], v[110:111], off
	v_lshlrev_b64 v[212:213], 12, v[108:109]
	v_lshl_add_u64 v[108:109], v[192:193], 0, v[212:213]
	global_load_dwordx4 v[160:163], v[108:109], off
	v_lshl_add_u64 v[108:109], v[194:195], 0, v[212:213]
	global_load_dwordx4 v[156:159], v[108:109], off
	v_or_b32_e32 v108, 32, v190
	v_ashrrev_i32_e32 v109, 31, v108
	v_lshlrev_b64 v[110:111], 6, v[108:109]
	v_lshlrev_b64 v[198:199], 12, v[108:109]
	v_lshl_add_u64 v[110:111], s[44:45], 0, v[110:111]
	v_lshl_add_u64 v[108:109], v[192:193], 0, v[198:199]
	global_load_dwordx4 v[152:155], v[110:111], off
	global_load_dwordx4 v[140:143], v[108:109], off
	v_lshl_add_u64 v[108:109], v[194:195], 0, v[198:199]
	global_load_dwordx4 v[136:139], v[108:109], off
	v_or_b32_e32 v108, 48, v190
	s_lshl_b32 s9, s38, 10
	v_ashrrev_i32_e32 v109, 31, v108
	s_add_i32 s9, s9, 0
	v_lshlrev_b64 v[110:111], 6, v[108:109]
	v_lshlrev_b64 v[196:197], 12, v[108:109]
	s_add_i32 s9, s9, 0x20000
	v_lshl_add_u64 v[110:111], s[44:45], 0, v[110:111]
	v_lshl_add_u64 v[108:109], v[192:193], 0, v[196:197]
	v_lshl_add_u32 v191, v221, 2, s9
	global_load_dwordx4 v[124:127], v[110:111], off
	global_load_dwordx4 v[112:115], v[108:109], off
	v_lshl_add_u64 v[108:109], v[194:195], 0, v[196:197]
	ds_read_b32 v226, v191 offset:64
	ds_read_b32 v227, v191 offset:128
	ds_read_b32 v228, v191 offset:192
	ds_read_b32 v229, v191 offset:512
	ds_read_b32 v230, v191 offset:576
	ds_read_b32 v231, v191 offset:640
	ds_read_b32 v232, v191 offset:704
	ds_read_b32 v191, v191
	s_mov_b32 s11, 0x358637bd
	global_load_dwordx4 v[108:111], v[108:109], off
	s_mov_b64 s[36:37], -1
	s_waitcnt lgkmcnt(0)
	v_mul_f32_e32 v224, 0xbfb8aa3b, v191
	v_pk_mul_f32 v[204:205], v[148:149], v[224:225] op_sel_hi:[1,0]
	s_andn2_b64 vcc, exec, s[2:3]
	v_readlane_b32 s17, v254, 6
	v_readlane_b32 s18, v254, 7
	v_readlane_b32 s19, v254, 8
	v_readlane_b32 s20, v254, 9
	v_readlane_b32 s21, v254, 10
	s_waitcnt vmcnt(0)
	v_ldexp_f32 v200, v200, -9
	v_ldexp_f32 v202, v202, -9
	v_ldexp_f32 v201, v201, -9
	v_ldexp_f32 v203, v203, -9
	v_fma_f32 v201, -v200, v200, v201
	v_fma_f32 v203, -v202, v202, v203
	v_max_f32_e32 v201, 0, v201
	v_max_f32_e32 v203, 0, v203
	v_add_f32_e32 v201, s11, v201
	v_add_f32_e32 v203, s11, v203
	v_rsq_f32_e32 v201, v201
	v_rsq_f32_e32 v203, v203
	s_mov_b32 s11, 0x358637bd
	v_mul_f32_e32 v216, v191, v201
	v_mul_f32_e32 v218, v191, v203
	v_mul_f32_e64 v220, v216, -v200
	v_mul_f32_e64 v222, v218, -v202
	v_lshlrev_b32_e32 v200, 16, v168
	v_and_b32_e32 v201, 0xffff0000, v168
	v_lshlrev_b32_e32 v202, 16, v172
	v_and_b32_e32 v203, 0xffff0000, v172
	v_min_f32_e32 v168, 0x42700000, v205
	v_min_f32_e32 v172, 0x42700000, v204
	v_pk_mul_f32 v[204:205], v[144:145], v[224:225] op_sel_hi:[1,0]
	v_pk_fma_f32 v[200:201], v[216:217], v[200:201], v[220:221] op_sel_hi:[0,1,0]
	v_min_f32_e32 v191, 0x42700000, v205
	v_min_f32_e32 v208, 0x42700000, v204
	v_exp_f32_e32 v204, v172
	v_exp_f32_e32 v205, v168
	v_exp_f32_e32 v208, v208
	v_exp_f32_e32 v209, v191
	v_pk_fma_f32 v[202:203], v[218:219], v[202:203], v[222:223] op_sel_hi:[0,1,0]
	v_pk_add_f32 v[204:205], v[204:205], 1.0 op_sel_hi:[1,0]
	v_pk_mul_f32 v[148:149], v[148:149], v[200:201]
	v_pk_add_f32 v[208:209], v[208:209], 1.0 op_sel_hi:[1,0]
	v_pk_mul_f32 v[144:145], v[144:145], v[202:203]
	v_pk_mul_f32 v[210:211], v[204:205], v[208:209]
	v_pk_mul_f32 v[148:149], v[148:149], v[208:209]
	v_lshlrev_b32_e32 v168, 16, v173
	v_pk_fma_f32 v[144:145], v[144:145], v[204:205], v[148:149]
	v_rcp_f32_e32 v148, v210
	v_rcp_f32_e32 v149, v211
	s_nop 0
	v_pk_mul_f32 v[144:145], v[144:145], v[148:149]
	v_lshlrev_b32_e32 v148, 16, v169
	v_and_b32_e32 v149, 0xffff0000, v169
	v_and_b32_e32 v169, 0xffff0000, v173
	v_pk_mul_f32 v[172:173], v[150:151], v[224:225] op_sel_hi:[1,0]
	v_pk_fma_f32 v[148:149], v[216:217], v[148:149], v[220:221] op_sel_hi:[0,1,0]
	v_min_f32_e32 v191, 0x42700000, v173
	v_min_f32_e32 v200, 0x42700000, v172
	v_pk_mul_f32 v[172:173], v[146:147], v[224:225] op_sel_hi:[1,0]
	v_pk_fma_f32 v[168:169], v[218:219], v[168:169], v[222:223] op_sel_hi:[0,1,0]
	v_min_f32_e32 v201, 0x42700000, v173
	v_min_f32_e32 v202, 0x42700000, v172
	v_exp_f32_e32 v172, v200
	v_exp_f32_e32 v173, v191
	v_exp_f32_e32 v200, v202
	v_exp_f32_e32 v201, v201
	v_pk_mul_f32 v[148:149], v[150:151], v[148:149]
	v_pk_add_f32 v[172:173], v[172:173], 1.0 op_sel_hi:[1,0]
	v_pk_mul_f32 v[146:147], v[146:147], v[168:169]
	v_pk_add_f32 v[200:201], v[200:201], 1.0 op_sel_hi:[1,0]
	v_pk_mul_f32 v[168:169], v[132:133], v[224:225] op_sel_hi:[1,0]
	v_pk_mul_f32 v[202:203], v[172:173], v[200:201]
;     __device__ __forceinline__ void operator()(const f32x4 (&acc)[2][2][4][2], const Unit& u, int wr, int wc, int fr, int fq) const {
;     ...
;                 stv[m] = *(const f32x4*)(ST + (size_t)row * 16 + head * 4); yfv[m] = *(const u32x4*)(Y + (size_t)row * 2048 + col0); ybv[m] = *(const u32x4*)(YB + (size_t)row * 2048 + col0); }
; #pragma unroll
;             for (int m = 0; m < 4; ++m) { const int row = row0 + ai * HALF + m * 16; const float r = tab[u.idx * 256 + (row & 255)];
;                 const f32x4 st = stv[m];
;                 const float muf = __builtin_amdgcn_ldexpf(st[0], -9), mub = __builtin_amdgcn_ldexpf(st[2], -9); float eps = 1e-6f; asm volatile("" : "+s"(eps));
;                 const float rf = __builtin_amdgcn_rsqf(fmaxf(__builtin_amdgcn_ldexpf(st[1], -9) - muf * muf, 0.f) + eps), rb = __builtin_amdgcn_rsqf(fmaxf(__builtin_amdgcn_ldexpf(st[3], -9) - mub * mub, 0.f) + eps);
;                 const float cf = rf * r, cb = rb * r, df = -muf * cf, db = -mub * cb, kr = -1.4426950409f * r;
;                 const u32x4 yfw = yfv[m], ybw = ybv[m];
;                 float o[8];
; #pragma unroll
;                 for (int n = 0; n < 2; ++n)
; #pragma unroll
;                     for (int e = 0; e < 4; e += 2) { const int q = n * 4 + e; const unsigned wf = yfw[q >> 1], wb = ybw[q >> 1];
;                         const f32x2 yf2 = {__builtin_bit_cast(float, wf << 16), __builtin_bit_cast(float, wf & 0xffff0000u)}, yb2 = {__builtin_bit_cast(float, wb << 16), __builtin_bit_cast(float, wb & 0xffff0000u)};
;                         const f32x2 af = {acc[ai][0][m][n][e], acc[ai][0][m][n][e + 1]}, ab = {acc[ai][1][m][n][e], acc[ai][1][m][n][e + 1]};
;                         const f32x2 nf = yf2 * cf + df, nb = yb2 * cb + db;
;                         const f32x2 xf = __builtin_elementwise_min(af * kr, (f32x2){60.f, 60.f}), xb = __builtin_elementwise_min(ab * kr, (f32x2){60.f, 60.f});
;                         const f32x2 pf = (f32x2){__builtin_amdgcn_exp2f(xf[0]), __builtin_amdgcn_exp2f(xf[1])} + 1.0f, pb = (f32x2){__builtin_amdgcn_exp2f(xb[0]), __builtin_amdgcn_exp2f(xb[1])} + 1.0f;
;                         const f32x2 den = pf * pb, num = (af * nf) * pb + (ab * nb) * pf;
;                         const f32x2 res = num * (f32x2){__builtin_amdgcn_rcpf(den[0]), __builtin_amdgcn_rcpf(den[1])};
;                         o[q] = res[0]; o[q + 1] = res[1]; }
	v_pk_mul_f32 v[148:149], v[148:149], v[200:201]
	v_lshlrev_b32_e32 v150, 16, v174
	v_pk_fma_f32 v[146:147], v[146:147], v[172:173], v[148:149]
	v_rcp_f32_e32 v148, v202
	v_rcp_f32_e32 v149, v203
	v_min_f32_e32 v172, 0x42700000, v168
	v_and_b32_e32 v151, 0xffff0000, v174
	v_pk_fma_f32 v[150:151], v[218:219], v[150:151], v[222:223] op_sel_hi:[0,1,0]
	v_pk_mul_f32 v[146:147], v[146:147], v[148:149]
	v_lshlrev_b32_e32 v148, 16, v170
	v_and_b32_e32 v149, 0xffff0000, v170
	v_min_f32_e32 v170, 0x42700000, v169
	v_pk_mul_f32 v[168:169], v[128:129], v[224:225] op_sel_hi:[1,0]
	v_pk_fma_f32 v[148:149], v[216:217], v[148:149], v[220:221] op_sel_hi:[0,1,0]
	v_min_f32_e32 v173, 0x42700000, v169
	v_min_f32_e32 v174, 0x42700000, v168
	v_exp_f32_e32 v168, v172
	v_exp_f32_e32 v169, v170
	v_exp_f32_e32 v172, v174
	v_exp_f32_e32 v173, v173
	v_pk_mul_f32 v[132:133], v[132:133], v[148:149]
	v_pk_add_f32 v[168:169], v[168:169], 1.0 op_sel_hi:[1,0]
	v_pk_mul_f32 v[128:129], v[128:129], v[150:151]
	v_pk_add_f32 v[172:173], v[172:173], 1.0 op_sel_hi:[1,0]
	v_pk_mul_f32 v[150:151], v[134:135], v[224:225] op_sel_hi:[1,0]
	v_pk_mul_f32 v[200:201], v[168:169], v[172:173]
	v_pk_mul_f32 v[132:133], v[132:133], v[172:173]
	v_lshlrev_b32_e32 v148, 16, v175
	v_pk_fma_f32 v[128:129], v[128:129], v[168:169], v[132:133]
	v_rcp_f32_e32 v132, v200
	v_rcp_f32_e32 v133, v201
	v_min_f32_e32 v168, 0x42700000, v151
	v_min_f32_e32 v169, 0x42700000, v150
	v_pk_mul_f32 v[150:151], v[130:131], v[224:225] op_sel_hi:[1,0]
	v_pk_mul_f32 v[132:133], v[128:129], v[132:133]
	v_lshlrev_b32_e32 v128, 16, v171
	v_and_b32_e32 v129, 0xffff0000, v171
	v_min_f32_e32 v170, 0x42700000, v151
	v_min_f32_e32 v171, 0x42700000, v150
	v_exp_f32_e32 v150, v169
	v_exp_f32_e32 v151, v168
	v_exp_f32_e32 v168, v171
	v_exp_f32_e32 v169, v170
	v_and_b32_e32 v149, 0xffff0000, v175
	v_pk_fma_f32 v[128:129], v[216:217], v[128:129], v[220:221] op_sel_hi:[0,1,0]
	v_pk_fma_f32 v[148:149], v[218:219], v[148:149], v[222:223] op_sel_hi:[0,1,0]
	v_pk_add_f32 v[150:151], v[150:151], 1.0 op_sel_hi:[1,0]
	v_pk_add_f32 v[168:169], v[168:169], 1.0 op_sel_hi:[1,0]
	v_pk_mul_f32 v[128:129], v[134:135], v[128:129]
	v_pk_mul_f32 v[170:171], v[150:151], v[168:169]
	v_pk_mul_f32 v[128:129], v[128:129], v[168:169]
	v_pk_mul_f32 v[130:131], v[130:131], v[148:149]
	v_lshlrev_b32_e32 v148, 16, v156
	v_pk_fma_f32 v[128:129], v[130:131], v[150:151], v[128:129]
	v_rcp_f32_e32 v130, v170
	v_rcp_f32_e32 v131, v171
	v_and_b32_e32 v149, 0xffff0000, v156
	v_pk_mul_f32 v[134:135], v[128:129], v[130:131]
	v_cvt_pk_bf16_f32 v128, v144, v145
	v_cvt_pk_bf16_f32 v129, v146, v147
	v_cvt_pk_bf16_f32 v130, v132, v133
	v_lshl_add_u64 v[132:133], s[4:5], 0, v[214:215]
	v_cvt_pk_bf16_f32 v131, v134, v135
	v_lshl_add_u64 v[132:133], v[132:133], 0, v[188:189]
	global_store_dwordx4 v[132:133], v[128:131], off
	v_add_u32_e32 v168, 0x80, v190
	v_ashrrev_i32_e32 v169, 31, v168
	v_lshlrev_b64 v[168:169], 6, v[168:169]
	v_lshl_add_u64 v[168:169], s[44:45], 0, v[168:169]
	global_load_dwordx4 v[168:171], v[168:169], off
	v_add_u32_e32 v172, 0x80, v190
	v_ashrrev_i32_e32 v173, 31, v172
	v_lshlrev_b64 v[172:173], 12, v[172:173]
	v_lshl_add_u64 v[172:173], v[192:193], 0, v[172:173]
	global_load_dwordx4 v[172:175], v[172:173], off
	v_add_u32_e32 v200, 0x80, v190
	v_ashrrev_i32_e32 v201, 31, v200
	v_lshlrev_b64 v[200:201], 12, v[200:201]
	v_lshl_add_u64 v[200:201], v[194:195], 0, v[200:201]
	global_load_dwordx4 v[200:203], v[200:201], off
	v_add_u32_e32 v208, 0x90, v190
	v_ashrrev_i32_e32 v209, 31, v208
	v_lshlrev_b64 v[208:209], 6, v[208:209]
	v_lshl_add_u64 v[208:209], s[44:45], 0, v[208:209]
	global_load_dwordx4 v[208:211], v[208:209], off
	v_ldexp_f32 v132, v167, -9
	v_lshlrev_b32_e32 v146, 16, v160
	v_ldexp_f32 v129, v164, -9
	v_ldexp_f32 v131, v166, -9
	v_ldexp_f32 v130, v165, -9
	v_bitop3_b32 v128, v190, s71, 16 bitop3:0xc8
	v_fma_f32 v130, -v129, v129, v130
	v_fma_f32 v132, -v131, v131, v132
	v_lshl_add_u32 v128, v128, 2, s9
	v_max_f32_e32 v130, 0, v130
	v_max_f32_e32 v132, 0, v132
	v_mov_b32_e32 v128, v226
	v_and_b32_e32 v147, 0xffff0000, v160
	v_add_f32_e32 v130, s11, v130
	v_add_f32_e32 v132, s11, v132
	v_rsq_f32_e32 v130, v130
	v_rsq_f32_e32 v132, v132
	s_movk_i32 s11, 0xef
	s_waitcnt lgkmcnt(0)
;     __device__ __forceinline__ void operator()(const f32x4 (&acc)[2][2][4][2], const Unit& u, int wr, int wc, int fr, int fq) const {
;     ...
;             for (int m = 0; m < 4; ++m) { const int row = row0 + ai * HALF + m * 16; const float r = tab[u.idx * 256 + (row & 255)];
;                 const f32x4 st = stv[m];
;                 const float muf = __builtin_amdgcn_ldexpf(st[0], -9), mub = __builtin_amdgcn_ldexpf(st[2], -9); float eps = 1e-6f; asm volatile("" : "+s"(eps));
;                 const float rf = __builtin_amdgcn_rsqf(fmaxf(__builtin_amdgcn_ldexpf(st[1], -9) - muf * muf, 0.f) + eps), rb = __builtin_amdgcn_rsqf(fmaxf(__builtin_amdgcn_ldexpf(st[3], -9) - mub * mub, 0.f) + eps);
;                 const float cf = rf * r, cb = rb * r, df = -muf * cf, db = -mub * cb, kr = -1.4426950409f * r;
;                 const u32x4 yfw = yfv[m], ybw = ybv[m];
;                 float o[8];
; #pragma unroll
;                 for (int n = 0; n < 2; ++n)
; #pragma unroll
;                     for (int e = 0; e < 4; e += 2) { const int q = n * 4 + e; const unsigned wf = yfw[q >> 1], wb = ybw[q >> 1];
;                         const f32x2 yf2 = {__builtin_bit_cast(float, wf << 16), __builtin_bit_cast(float, wf & 0xffff0000u)}, yb2 = {__builtin_bit_cast(float, wb << 16), __builtin_bit_cast(float, wb & 0xffff0000u)};
;                         const f32x2 af = {acc[ai][0][m][n][e], acc[ai][0][m][n][e + 1]}, ab = {acc[ai][1][m][n][e], acc[ai][1][m][n][e + 1]};
;                         const f32x2 nf = yf2 * cf + df, nb = yb2 * cb + db;
;                         const f32x2 xf = __builtin_elementwise_min(af * kr, (f32x2){60.f, 60.f}), xb = __builtin_elementwise_min(ab * kr, (f32x2){60.f, 60.f});
;                         const f32x2 pf = (f32x2){__builtin_amdgcn_exp2f(xf[0]), __builtin_amdgcn_exp2f(xf[1])} + 1.0f, pb = (f32x2){__builtin_amdgcn_exp2f(xb[0]), __builtin_amdgcn_exp2f(xb[1])} + 1.0f;
;                         const f32x2 den = pf * pb, num = (af * nf) * pb + (ab * nb) * pf;
;                         const f32x2 res = num * (f32x2){__builtin_amdgcn_rcpf(den[0]), __builtin_amdgcn_rcpf(den[1])};
;                         o[q] = res[0]; o[q + 1] = res[1]; }
;                 u32x4 w; w.x = cvt_pk_bf16(o[0], o[1]); w.y = cvt_pk_bf16(o[2], o[3]); w.z = cvt_pk_bf16(o[4], o[5]); w.w = cvt_pk_bf16(o[6], o[7]);
	v_mul_f32_e32 v130, v128, v130
	v_mul_f32_e32 v132, v128, v132
	v_mul_f32_e32 v128, 0xbfb8aa3b, v128
	v_pk_mul_f32 v[150:151], v[120:121], v[128:129] op_sel_hi:[1,0]
	v_mul_f32_e64 v134, v130, -v129
	v_min_f32_e32 v129, 0x42700000, v151
	v_mul_f32_e64 v144, v132, -v131
	v_pk_fma_f32 v[146:147], v[130:131], v[146:147], v[134:135] op_sel_hi:[0,1,0]
	v_min_f32_e32 v131, 0x42700000, v150
	v_pk_mul_f32 v[150:151], v[116:117], v[128:129] op_sel_hi:[1,0]
	v_pk_fma_f32 v[148:149], v[132:133], v[148:149], v[144:145] op_sel_hi:[0,1,0]
	v_min_f32_e32 v133, 0x42700000, v151
	v_min_f32_e32 v135, 0x42700000, v150
	v_exp_f32_e32 v150, v131
	v_exp_f32_e32 v151, v129
	v_exp_f32_e32 v164, v135
	v_exp_f32_e32 v165, v133
	v_pk_mul_f32 v[120:121], v[120:121], v[146:147]
	v_pk_add_f32 v[150:151], v[150:151], 1.0 op_sel_hi:[1,0]
	v_pk_mul_f32 v[116:117], v[116:117], v[148:149]
	v_pk_add_f32 v[164:165], v[164:165], 1.0 op_sel_hi:[1,0]
	v_pk_mul_f32 v[148:149], v[122:123], v[128:129] op_sel_hi:[1,0]
	v_pk_mul_f32 v[166:167], v[150:151], v[164:165]
	v_pk_mul_f32 v[120:121], v[120:121], v[164:165]
	v_min_f32_e32 v129, 0x42700000, v149
	v_pk_fma_f32 v[116:117], v[116:117], v[150:151], v[120:121]
	v_rcp_f32_e32 v120, v166
	v_rcp_f32_e32 v121, v167
	v_lshlrev_b32_e32 v146, 16, v157
	v_and_b32_e32 v147, 0xffff0000, v157
	v_pk_fma_f32 v[146:147], v[132:133], v[146:147], v[144:145] op_sel_hi:[0,1,0]
	v_pk_mul_f32 v[116:117], v[116:117], v[120:121]
	v_lshlrev_b32_e32 v120, 16, v161
	v_and_b32_e32 v121, 0xffff0000, v161
	v_pk_fma_f32 v[120:121], v[130:131], v[120:121], v[134:135] op_sel_hi:[0,1,0]
	v_min_f32_e32 v131, 0x42700000, v148
	v_pk_mul_f32 v[148:149], v[118:119], v[128:129] op_sel_hi:[1,0]
	v_pk_mul_f32 v[120:121], v[122:123], v[120:121]
	v_min_f32_e32 v133, 0x42700000, v149
	v_min_f32_e32 v135, 0x42700000, v148
	v_exp_f32_e32 v148, v131
	v_exp_f32_e32 v149, v129
	v_exp_f32_e32 v150, v135
	v_exp_f32_e32 v151, v133
	v_pk_mul_f32 v[118:119], v[118:119], v[146:147]
	v_pk_add_f32 v[148:149], v[148:149], 1.0 op_sel_hi:[1,0]
	v_pk_mul_f32 v[146:147], v[104:105], v[128:129] op_sel_hi:[1,0]
	v_pk_add_f32 v[150:151], v[150:151], 1.0 op_sel_hi:[1,0]
	v_min_f32_e32 v129, 0x42700000, v147
	v_pk_mul_f32 v[156:157], v[148:149], v[150:151]
	v_pk_mul_f32 v[120:121], v[120:121], v[150:151]
	v_lshlrev_b32_e32 v122, 16, v158
	v_pk_fma_f32 v[118:119], v[118:119], v[148:149], v[120:121]
	v_rcp_f32_e32 v120, v156
	v_rcp_f32_e32 v121, v157
	v_and_b32_e32 v123, 0xffff0000, v158
	v_pk_fma_f32 v[122:123], v[132:133], v[122:123], v[144:145] op_sel_hi:[0,1,0]
	v_pk_mul_f32 v[118:119], v[118:119], v[120:121]
	v_lshlrev_b32_e32 v120, 16, v162
	v_and_b32_e32 v121, 0xffff0000, v162
	v_pk_fma_f32 v[120:121], v[130:131], v[120:121], v[134:135] op_sel_hi:[0,1,0]
	v_min_f32_e32 v131, 0x42700000, v146
	v_pk_mul_f32 v[146:147], v[100:101], v[128:129] op_sel_hi:[1,0]
	v_pk_mul_f32 v[104:105], v[104:105], v[120:121]
	v_min_f32_e32 v133, 0x42700000, v147
	v_min_f32_e32 v135, 0x42700000, v146
	v_exp_f32_e32 v146, v131
	v_exp_f32_e32 v147, v129
	v_exp_f32_e32 v148, v135
	v_exp_f32_e32 v149, v133
	v_pk_mul_f32 v[100:101], v[100:101], v[122:123]
	v_pk_add_f32 v[146:147], v[146:147], 1.0 op_sel_hi:[1,0]
	v_pk_mul_f32 v[122:123], v[106:107], v[128:129] op_sel_hi:[1,0]
	v_pk_add_f32 v[148:149], v[148:149], 1.0 op_sel_hi:[1,0]
	v_min_f32_e32 v129, 0x42700000, v123
	v_pk_mul_f32 v[150:151], v[146:147], v[148:149]
	v_pk_mul_f32 v[104:105], v[104:105], v[148:149]
	v_lshlrev_b32_e32 v120, 16, v159
	v_pk_fma_f32 v[100:101], v[100:101], v[146:147], v[104:105]
	v_rcp_f32_e32 v104, v150
	v_rcp_f32_e32 v105, v151
	v_and_b32_e32 v121, 0xffff0000, v159
	v_pk_fma_f32 v[120:121], v[132:133], v[120:121], v[144:145] op_sel_hi:[0,1,0]
	v_pk_mul_f32 v[104:105], v[100:101], v[104:105]
	v_lshlrev_b32_e32 v100, 16, v163
	v_and_b32_e32 v101, 0xffff0000, v163
	v_pk_fma_f32 v[100:101], v[130:131], v[100:101], v[134:135] op_sel_hi:[0,1,0]
	v_min_f32_e32 v130, 0x42700000, v122
	v_pk_mul_f32 v[122:123], v[102:103], v[128:129] op_sel_hi:[1,0]
	v_pk_mul_f32 v[100:101], v[106:107], v[100:101]
	v_min_f32_e32 v131, 0x42700000, v123
	v_min_f32_e32 v128, 0x42700000, v122
	v_exp_f32_e32 v122, v130
	v_exp_f32_e32 v123, v129
	v_exp_f32_e32 v128, v128
	v_exp_f32_e32 v129, v131
	v_pk_mul_f32 v[102:103], v[102:103], v[120:121]
	v_pk_add_f32 v[122:123], v[122:123], 1.0 op_sel_hi:[1,0]
	v_lshlrev_b32_e32 v120, 16, v136
	v_pk_add_f32 v[128:129], v[128:129], 1.0 op_sel_hi:[1,0]
	v_and_b32_e32 v121, 0xffff0000, v136
	v_pk_mul_f32 v[130:131], v[122:123], v[128:129]
	v_pk_mul_f32 v[100:101], v[100:101], v[128:129]
	s_nop 0
	v_pk_fma_f32 v[100:101], v[102:103], v[122:123], v[100:101]
	v_rcp_f32_e32 v102, v130
	v_rcp_f32_e32 v103, v131
	s_nop 0
	v_pk_mul_f32 v[106:107], v[100:101], v[102:103]
	v_cvt_pk_bf16_f32 v100, v116, v117
	v_cvt_pk_bf16_f32 v101, v118, v119
	v_cvt_pk_bf16_f32 v102, v104, v105
	v_lshl_add_u64 v[104:105], s[4:5], 0, v[212:213]
	v_cvt_pk_bf16_f32 v103, v106, v107
	v_lshl_add_u64 v[104:105], v[104:105], 0, v[188:189]
	global_store_dwordx4 v[104:105], v[100:103], off
	v_add_u32_e32 v156, 0x90, v190
	v_ashrrev_i32_e32 v157, 31, v156
	v_lshlrev_b64 v[156:157], 12, v[156:157]
	v_lshl_add_u64 v[156:157], v[192:193], 0, v[156:157]
	global_load_dwordx4 v[156:159], v[156:157], off
	v_add_u32_e32 v160, 0x90, v190
	v_ashrrev_i32_e32 v161, 31, v160
	v_lshlrev_b64 v[160:161], 12, v[160:161]
	v_lshl_add_u64 v[160:161], v[194:195], 0, v[160:161]
	global_load_dwordx4 v[160:163], v[160:161], off
	v_add_u32_e32 v164, 0xa0, v190
	v_ashrrev_i32_e32 v165, 31, v164
	v_lshlrev_b64 v[164:165], 6, v[164:165]
	v_lshl_add_u64 v[164:165], s[44:45], 0, v[164:165]
	global_load_dwordx4 v[164:167], v[164:165], off
	v_add_u32_e32 v148, 0xa0, v190
	v_ashrrev_i32_e32 v149, 31, v148
	v_lshlrev_b64 v[148:149], 12, v[148:149]
	v_lshl_add_u64 v[148:149], v[192:193], 0, v[148:149]
	global_load_dwordx4 v[148:151], v[148:149], off
	v_add_u32_e32 v212, 0xa0, v190
	v_ashrrev_i32_e32 v213, 31, v212
	v_lshlrev_b64 v[212:213], 12, v[212:213]
	v_lshl_add_u64 v[212:213], v[194:195], 0, v[212:213]
	global_load_dwordx4 v[212:215], v[212:213], off
	v_ldexp_f32 v104, v155, -9
	v_lshlrev_b32_e32 v118, 16, v140
	v_ldexp_f32 v101, v152, -9
	v_ldexp_f32 v103, v154, -9
	v_ldexp_f32 v102, v153, -9
	v_bitop3_b32 v100, v190, s11, 32 bitop3:0xc8
	v_fma_f32 v102, -v101, v101, v102
	v_fma_f32 v104, -v103, v103, v104
	v_lshl_add_u32 v100, v100, 2, s9
	s_mov_b32 s11, 0x358637bd
	v_max_f32_e32 v102, 0, v102
	v_max_f32_e32 v104, 0, v104
	v_mov_b32_e32 v100, v227
	v_and_b32_e32 v119, 0xffff0000, v140
	v_add_f32_e32 v102, s11, v102
	v_add_f32_e32 v104, s11, v104
	v_rsq_f32_e32 v102, v102
	v_rsq_f32_e32 v104, v104
	s_mov_b32 s11, 0x358637bd
	s_waitcnt lgkmcnt(0)
;     __device__ __forceinline__ void operator()(const f32x4 (&acc)[2][2][4][2], const Unit& u, int wr, int wc, int fr, int fq) const {
;     ...
;             for (int m = 0; m < 4; ++m) { const int row = row0 + ai * HALF + m * 16; const float r = tab[u.idx * 256 + (row & 255)];
;                 const f32x4 st = stv[m];
;                 const float muf = __builtin_amdgcn_ldexpf(st[0], -9), mub = __builtin_amdgcn_ldexpf(st[2], -9); float eps = 1e-6f; asm volatile("" : "+s"(eps));
;                 const float rf = __builtin_amdgcn_rsqf(fmaxf(__builtin_amdgcn_ldexpf(st[1], -9) - muf * muf, 0.f) + eps), rb = __builtin_amdgcn_rsqf(fmaxf(__builtin_amdgcn_ldexpf(st[3], -9) - mub * mub, 0.f) + eps);
;                 const float cf = rf * r, cb = rb * r, df = -muf * cf, db = -mub * cb, kr = -1.4426950409f * r;
;                 const u32x4 yfw = yfv[m], ybw = ybv[m];
;                 float o[8];
; #pragma unroll
;                 for (int n = 0; n < 2; ++n)
; #pragma unroll
;                     for (int e = 0; e < 4; e += 2) { const int q = n * 4 + e; const unsigned wf = yfw[q >> 1], wb = ybw[q >> 1];
;                         const f32x2 yf2 = {__builtin_bit_cast(float, wf << 16), __builtin_bit_cast(float, wf & 0xffff0000u)}, yb2 = {__builtin_bit_cast(float, wb << 16), __builtin_bit_cast(float, wb & 0xffff0000u)};
;                         const f32x2 af = {acc[ai][0][m][n][e], acc[ai][0][m][n][e + 1]}, ab = {acc[ai][1][m][n][e], acc[ai][1][m][n][e + 1]};
;                         const f32x2 nf = yf2 * cf + df, nb = yb2 * cb + db;
;                         const f32x2 xf = __builtin_elementwise_min(af * kr, (f32x2){60.f, 60.f}), xb = __builtin_elementwise_min(ab * kr, (f32x2){60.f, 60.f});
;                         const f32x2 pf = (f32x2){__builtin_amdgcn_exp2f(xf[0]), __builtin_amdgcn_exp2f(xf[1])} + 1.0f, pb = (f32x2){__builtin_amdgcn_exp2f(xb[0]), __builtin_amdgcn_exp2f(xb[1])} + 1.0f;
;                         const f32x2 den = pf * pb, num = (af * nf) * pb + (ab * nb) * pf;
;                         const f32x2 res = num * (f32x2){__builtin_amdgcn_rcpf(den[0]), __builtin_amdgcn_rcpf(den[1])};
;                         o[q] = res[0]; o[q + 1] = res[1]; }
;                 u32x4 w; w.x = cvt_pk_bf16(o[0], o[1]); w.y = cvt_pk_bf16(o[2], o[3]); w.z = cvt_pk_bf16(o[4], o[5]); w.w = cvt_pk_bf16(o[6], o[7]);
	v_mul_f32_e32 v102, v100, v102
	v_mul_f32_e32 v104, v100, v104
	v_mul_f32_e32 v100, 0xbfb8aa3b, v100
	v_pk_mul_f32 v[122:123], v[96:97], v[100:101] op_sel_hi:[1,0]
	v_mul_f32_e64 v106, v102, -v101
	v_min_f32_e32 v101, 0x42700000, v123
	v_mul_f32_e64 v116, v104, -v103
	v_pk_fma_f32 v[118:119], v[102:103], v[118:119], v[106:107] op_sel_hi:[0,1,0]
	v_min_f32_e32 v103, 0x42700000, v122
	v_pk_mul_f32 v[122:123], v[92:93], v[100:101] op_sel_hi:[1,0]
	v_pk_fma_f32 v[120:121], v[104:105], v[120:121], v[116:117] op_sel_hi:[0,1,0]
	v_min_f32_e32 v105, 0x42700000, v123
	v_min_f32_e32 v107, 0x42700000, v122
	v_exp_f32_e32 v122, v103
	v_exp_f32_e32 v123, v101
	v_exp_f32_e32 v128, v107
	v_exp_f32_e32 v129, v105
	v_pk_mul_f32 v[96:97], v[96:97], v[118:119]
	v_pk_add_f32 v[122:123], v[122:123], 1.0 op_sel_hi:[1,0]
	v_pk_mul_f32 v[92:93], v[92:93], v[120:121]
	v_pk_add_f32 v[128:129], v[128:129], 1.0 op_sel_hi:[1,0]
	v_pk_mul_f32 v[120:121], v[98:99], v[100:101] op_sel_hi:[1,0]
	v_pk_mul_f32 v[130:131], v[122:123], v[128:129]
	v_pk_mul_f32 v[96:97], v[96:97], v[128:129]
	v_min_f32_e32 v101, 0x42700000, v121
	v_pk_fma_f32 v[92:93], v[92:93], v[122:123], v[96:97]
	v_rcp_f32_e32 v96, v130
	v_rcp_f32_e32 v97, v131
	v_lshlrev_b32_e32 v118, 16, v137
	v_and_b32_e32 v119, 0xffff0000, v137
	v_pk_fma_f32 v[118:119], v[104:105], v[118:119], v[116:117] op_sel_hi:[0,1,0]
	v_pk_mul_f32 v[92:93], v[92:93], v[96:97]
	v_lshlrev_b32_e32 v96, 16, v141
	v_and_b32_e32 v97, 0xffff0000, v141
	v_pk_fma_f32 v[96:97], v[102:103], v[96:97], v[106:107] op_sel_hi:[0,1,0]
	v_min_f32_e32 v103, 0x42700000, v120
	v_pk_mul_f32 v[120:121], v[94:95], v[100:101] op_sel_hi:[1,0]
	v_pk_mul_f32 v[96:97], v[98:99], v[96:97]
	v_min_f32_e32 v105, 0x42700000, v121
	v_min_f32_e32 v107, 0x42700000, v120
	v_exp_f32_e32 v120, v103
	v_exp_f32_e32 v121, v101
	v_exp_f32_e32 v122, v107
	v_exp_f32_e32 v123, v105
	v_pk_mul_f32 v[94:95], v[94:95], v[118:119]
	v_pk_add_f32 v[120:121], v[120:121], 1.0 op_sel_hi:[1,0]
	v_pk_mul_f32 v[118:119], v[88:89], v[100:101] op_sel_hi:[1,0]
	v_pk_add_f32 v[122:123], v[122:123], 1.0 op_sel_hi:[1,0]
	v_min_f32_e32 v101, 0x42700000, v119
	v_pk_mul_f32 v[128:129], v[120:121], v[122:123]
	v_pk_mul_f32 v[96:97], v[96:97], v[122:123]
	v_lshlrev_b32_e32 v98, 16, v138
	v_pk_fma_f32 v[94:95], v[94:95], v[120:121], v[96:97]
	v_rcp_f32_e32 v96, v128
	v_rcp_f32_e32 v97, v129
	v_and_b32_e32 v99, 0xffff0000, v138
	v_pk_fma_f32 v[98:99], v[104:105], v[98:99], v[116:117] op_sel_hi:[0,1,0]
	v_add_u32_e32 v130, 0x80, v190
	v_pk_mul_f32 v[94:95], v[94:95], v[96:97]
	v_lshlrev_b32_e32 v96, 16, v142
	v_and_b32_e32 v97, 0xffff0000, v142
	v_pk_fma_f32 v[96:97], v[102:103], v[96:97], v[106:107] op_sel_hi:[0,1,0]
	v_min_f32_e32 v103, 0x42700000, v118
	v_pk_mul_f32 v[118:119], v[84:85], v[100:101] op_sel_hi:[1,0]
	v_pk_mul_f32 v[88:89], v[88:89], v[96:97]
	v_min_f32_e32 v105, 0x42700000, v119
	v_min_f32_e32 v107, 0x42700000, v118
	v_exp_f32_e32 v118, v103
	v_exp_f32_e32 v119, v101
	v_exp_f32_e32 v120, v107
	v_exp_f32_e32 v121, v105
	v_pk_mul_f32 v[84:85], v[84:85], v[98:99]
	v_pk_add_f32 v[118:119], v[118:119], 1.0 op_sel_hi:[1,0]
	v_pk_mul_f32 v[98:99], v[90:91], v[100:101] op_sel_hi:[1,0]
	v_pk_add_f32 v[120:121], v[120:121], 1.0 op_sel_hi:[1,0]
	v_min_f32_e32 v101, 0x42700000, v99
	v_pk_mul_f32 v[122:123], v[118:119], v[120:121]
	v_pk_mul_f32 v[88:89], v[88:89], v[120:121]
	v_lshlrev_b32_e32 v96, 16, v139
	v_pk_fma_f32 v[84:85], v[84:85], v[118:119], v[88:89]
	v_rcp_f32_e32 v88, v122
	v_rcp_f32_e32 v89, v123
	v_and_b32_e32 v97, 0xffff0000, v139
	v_pk_fma_f32 v[96:97], v[104:105], v[96:97], v[116:117] op_sel_hi:[0,1,0]
	v_ashrrev_i32_e32 v131, 31, v130
	v_pk_mul_f32 v[88:89], v[84:85], v[88:89]
	v_lshlrev_b32_e32 v84, 16, v143
	v_and_b32_e32 v85, 0xffff0000, v143
	v_pk_fma_f32 v[84:85], v[102:103], v[84:85], v[106:107] op_sel_hi:[0,1,0]
	v_min_f32_e32 v102, 0x42700000, v98
	v_pk_mul_f32 v[98:99], v[86:87], v[100:101] op_sel_hi:[1,0]
	v_pk_mul_f32 v[84:85], v[90:91], v[84:85]
	v_min_f32_e32 v103, 0x42700000, v99
	v_min_f32_e32 v100, 0x42700000, v98
	v_exp_f32_e32 v98, v102
	v_exp_f32_e32 v99, v101
	v_exp_f32_e32 v100, v100
	v_exp_f32_e32 v101, v103
	v_pk_mul_f32 v[86:87], v[86:87], v[96:97]
	v_pk_add_f32 v[98:99], v[98:99], 1.0 op_sel_hi:[1,0]
	v_lshlrev_b32_e32 v96, 16, v108
	v_pk_add_f32 v[100:101], v[100:101], 1.0 op_sel_hi:[1,0]
	v_and_b32_e32 v97, 0xffff0000, v108
	v_pk_mul_f32 v[102:103], v[98:99], v[100:101]
	v_pk_mul_f32 v[84:85], v[84:85], v[100:101]
	v_lshlrev_b64 v[122:123], 12, v[130:131]
	v_pk_fma_f32 v[84:85], v[86:87], v[98:99], v[84:85]
	v_rcp_f32_e32 v86, v102
	v_rcp_f32_e32 v87, v103
	v_add_u32_e32 v120, 0xa0, v190
	v_ashrrev_i32_e32 v121, 31, v120
	v_add_u32_e32 v116, 0xb0, v190
	v_pk_mul_f32 v[90:91], v[84:85], v[86:87]
	v_cvt_pk_bf16_f32 v84, v92, v93
	v_cvt_pk_bf16_f32 v85, v94, v95
	v_cvt_pk_bf16_f32 v86, v88, v89
	v_lshl_add_u64 v[88:89], s[4:5], 0, v[198:199]
	v_cvt_pk_bf16_f32 v87, v90, v91
	v_lshl_add_u64 v[88:89], v[88:89], 0, v[188:189]
	global_store_dwordx4 v[88:89], v[84:87], off
	v_add_u32_e32 v152, 0xb0, v190
	v_ashrrev_i32_e32 v153, 31, v152
	v_lshlrev_b64 v[152:153], 6, v[152:153]
	v_lshl_add_u64 v[152:153], s[44:45], 0, v[152:153]
	global_load_dwordx4 v[152:155], v[152:153], off
	v_ldexp_f32 v88, v127, -9
	v_lshlrev_b32_e32 v94, 16, v112
	v_ldexp_f32 v85, v124, -9
	v_ldexp_f32 v87, v126, -9
	v_ldexp_f32 v86, v125, -9
	v_bitop3_b32 v84, v190, s70, 48 bitop3:0xc8
	v_fma_f32 v86, -v85, v85, v86
	v_fma_f32 v88, -v87, v87, v88
	v_lshl_add_u32 v84, v84, 2, s9
	v_max_f32_e32 v86, 0, v86
	v_max_f32_e32 v88, 0, v88
	v_mov_b32_e32 v84, v228
	v_and_b32_e32 v95, 0xffff0000, v112
	v_add_f32_e32 v86, s11, v86
	v_add_f32_e32 v88, s11, v88
	v_rsq_f32_e32 v86, v86
	v_rsq_f32_e32 v88, v88
	v_add_u32_e32 v124, 0x90, v190
	v_ashrrev_i32_e32 v125, 31, v124
	s_waitcnt lgkmcnt(0)
;     __device__ __forceinline__ void operator()(const f32x4 (&acc)[2][2][4][2], const Unit& u, int wr, int wc, int fr, int fq) const {
;     ...
;             for (int m = 0; m < 4; ++m) { const int row = row0 + ai * HALF + m * 16; const float r = tab[u.idx * 256 + (row & 255)];
;                 const f32x4 st = stv[m];
;                 const float muf = __builtin_amdgcn_ldexpf(st[0], -9), mub = __builtin_amdgcn_ldexpf(st[2], -9); float eps = 1e-6f; asm volatile("" : "+s"(eps));
;                 const float rf = __builtin_amdgcn_rsqf(fmaxf(__builtin_amdgcn_ldexpf(st[1], -9) - muf * muf, 0.f) + eps), rb = __builtin_amdgcn_rsqf(fmaxf(__builtin_amdgcn_ldexpf(st[3], -9) - mub * mub, 0.f) + eps);
;                 const float cf = rf * r, cb = rb * r, df = -muf * cf, db = -mub * cb, kr = -1.4426950409f * r;
;                 const u32x4 yfw = yfv[m], ybw = ybv[m];
;                 float o[8];
; #pragma unroll
;                 for (int n = 0; n < 2; ++n)
; #pragma unroll
;                     for (int e = 0; e < 4; e += 2) { const int q = n * 4 + e; const unsigned wf = yfw[q >> 1], wb = ybw[q >> 1];
;                         const f32x2 yf2 = {__builtin_bit_cast(float, wf << 16), __builtin_bit_cast(float, wf & 0xffff0000u)}, yb2 = {__builtin_bit_cast(float, wb << 16), __builtin_bit_cast(float, wb & 0xffff0000u)};
;                         const f32x2 af = {acc[ai][0][m][n][e], acc[ai][0][m][n][e + 1]}, ab = {acc[ai][1][m][n][e], acc[ai][1][m][n][e + 1]};
;                         const f32x2 nf = yf2 * cf + df, nb = yb2 * cb + db;
;                         const f32x2 xf = __builtin_elementwise_min(af * kr, (f32x2){60.f, 60.f}), xb = __builtin_elementwise_min(ab * kr, (f32x2){60.f, 60.f});
;                         const f32x2 pf = (f32x2){__builtin_amdgcn_exp2f(xf[0]), __builtin_amdgcn_exp2f(xf[1])} + 1.0f, pb = (f32x2){__builtin_amdgcn_exp2f(xb[0]), __builtin_amdgcn_exp2f(xb[1])} + 1.0f;
;                         const f32x2 den = pf * pb, num = (af * nf) * pb + (ab * nb) * pf;
;                         const f32x2 res = num * (f32x2){__builtin_amdgcn_rcpf(den[0]), __builtin_amdgcn_rcpf(den[1])};
;                         o[q] = res[0]; o[q + 1] = res[1]; }
;                 u32x4 w; w.x = cvt_pk_bf16(o[0], o[1]); w.y = cvt_pk_bf16(o[2], o[3]); w.z = cvt_pk_bf16(o[4], o[5]); w.w = cvt_pk_bf16(o[6], o[7]);
	v_mul_f32_e32 v86, v84, v86
	v_mul_f32_e32 v88, v84, v88
	v_mul_f32_e32 v84, 0xbfb8aa3b, v84
	v_pk_mul_f32 v[98:99], v[80:81], v[84:85] op_sel_hi:[1,0]
	v_mul_f32_e64 v90, v86, -v85
	v_min_f32_e32 v85, 0x42700000, v99
	v_mul_f32_e64 v92, v88, -v87
	v_pk_fma_f32 v[94:95], v[86:87], v[94:95], v[90:91] op_sel_hi:[0,1,0]
	v_min_f32_e32 v87, 0x42700000, v98
	v_pk_mul_f32 v[98:99], v[76:77], v[84:85] op_sel_hi:[1,0]
	v_pk_fma_f32 v[96:97], v[88:89], v[96:97], v[92:93] op_sel_hi:[0,1,0]
	v_min_f32_e32 v89, 0x42700000, v99
	v_min_f32_e32 v91, 0x42700000, v98
	v_exp_f32_e32 v98, v87
	v_exp_f32_e32 v99, v85
	v_exp_f32_e32 v100, v91
	v_exp_f32_e32 v101, v89
	v_pk_mul_f32 v[80:81], v[80:81], v[94:95]
	v_pk_add_f32 v[98:99], v[98:99], 1.0 op_sel_hi:[1,0]
	v_pk_mul_f32 v[76:77], v[76:77], v[96:97]
	v_pk_add_f32 v[100:101], v[100:101], 1.0 op_sel_hi:[1,0]
	v_pk_mul_f32 v[96:97], v[82:83], v[84:85] op_sel_hi:[1,0]
	v_pk_mul_f32 v[102:103], v[98:99], v[100:101]
	v_pk_mul_f32 v[80:81], v[80:81], v[100:101]
	v_min_f32_e32 v85, 0x42700000, v97
	v_pk_fma_f32 v[76:77], v[76:77], v[98:99], v[80:81]
	v_rcp_f32_e32 v80, v102
	v_rcp_f32_e32 v81, v103
	v_lshlrev_b32_e32 v94, 16, v109
	v_and_b32_e32 v95, 0xffff0000, v109
	v_pk_fma_f32 v[94:95], v[88:89], v[94:95], v[92:93] op_sel_hi:[0,1,0]
	v_pk_mul_f32 v[76:77], v[76:77], v[80:81]
	v_lshlrev_b32_e32 v80, 16, v113
	v_and_b32_e32 v81, 0xffff0000, v113
	v_pk_fma_f32 v[80:81], v[86:87], v[80:81], v[90:91] op_sel_hi:[0,1,0]
	v_min_f32_e32 v87, 0x42700000, v96
	v_pk_mul_f32 v[96:97], v[78:79], v[84:85] op_sel_hi:[1,0]
	v_pk_mul_f32 v[80:81], v[82:83], v[80:81]
	v_min_f32_e32 v89, 0x42700000, v97
	v_min_f32_e32 v91, 0x42700000, v96
	v_exp_f32_e32 v96, v87
	v_exp_f32_e32 v97, v85
	v_exp_f32_e32 v98, v91
	v_exp_f32_e32 v99, v89
	v_pk_mul_f32 v[78:79], v[78:79], v[94:95]
	v_pk_add_f32 v[96:97], v[96:97], 1.0 op_sel_hi:[1,0]
	v_pk_mul_f32 v[94:95], v[72:73], v[84:85] op_sel_hi:[1,0]
	v_pk_add_f32 v[98:99], v[98:99], 1.0 op_sel_hi:[1,0]
	v_min_f32_e32 v85, 0x42700000, v95
	v_pk_mul_f32 v[100:101], v[96:97], v[98:99]
	v_pk_mul_f32 v[80:81], v[80:81], v[98:99]
	v_lshlrev_b32_e32 v82, 16, v110
	v_pk_fma_f32 v[78:79], v[78:79], v[96:97], v[80:81]
	v_rcp_f32_e32 v80, v100
	v_rcp_f32_e32 v81, v101
	v_and_b32_e32 v83, 0xffff0000, v110
	v_pk_fma_f32 v[82:83], v[88:89], v[82:83], v[92:93] op_sel_hi:[0,1,0]
	v_lshlrev_b64 v[118:119], 12, v[124:125]
	v_pk_mul_f32 v[78:79], v[78:79], v[80:81]
	v_lshlrev_b32_e32 v80, 16, v114
	v_and_b32_e32 v81, 0xffff0000, v114
	v_pk_fma_f32 v[80:81], v[86:87], v[80:81], v[90:91] op_sel_hi:[0,1,0]
	v_min_f32_e32 v87, 0x42700000, v94
	v_pk_mul_f32 v[94:95], v[68:69], v[84:85] op_sel_hi:[1,0]
	v_pk_mul_f32 v[72:73], v[72:73], v[80:81]
	v_min_f32_e32 v89, 0x42700000, v95
	v_min_f32_e32 v91, 0x42700000, v94
	v_exp_f32_e32 v94, v87
	v_exp_f32_e32 v95, v85
	v_exp_f32_e32 v96, v91
	v_exp_f32_e32 v97, v89
	v_pk_mul_f32 v[68:69], v[68:69], v[82:83]
	v_pk_add_f32 v[94:95], v[94:95], 1.0 op_sel_hi:[1,0]
	v_pk_mul_f32 v[82:83], v[74:75], v[84:85] op_sel_hi:[1,0]
	v_pk_add_f32 v[96:97], v[96:97], 1.0 op_sel_hi:[1,0]
	v_min_f32_e32 v85, 0x42700000, v83
	v_pk_mul_f32 v[98:99], v[94:95], v[96:97]
	v_pk_mul_f32 v[72:73], v[72:73], v[96:97]
	v_lshlrev_b32_e32 v80, 16, v111
	v_pk_fma_f32 v[68:69], v[68:69], v[94:95], v[72:73]
	v_rcp_f32_e32 v72, v98
	v_rcp_f32_e32 v73, v99
	v_and_b32_e32 v81, 0xffff0000, v111
	v_pk_fma_f32 v[80:81], v[88:89], v[80:81], v[92:93] op_sel_hi:[0,1,0]
	v_ashrrev_i32_e32 v117, 31, v116
	v_pk_mul_f32 v[72:73], v[68:69], v[72:73]
	v_lshlrev_b32_e32 v68, 16, v115
	v_and_b32_e32 v69, 0xffff0000, v115
	v_pk_fma_f32 v[68:69], v[86:87], v[68:69], v[90:91] op_sel_hi:[0,1,0]
	v_min_f32_e32 v86, 0x42700000, v82
	v_pk_mul_f32 v[82:83], v[70:71], v[84:85] op_sel_hi:[1,0]
	v_pk_mul_f32 v[68:69], v[74:75], v[68:69]
	v_min_f32_e32 v87, 0x42700000, v83
	v_min_f32_e32 v84, 0x42700000, v82
	v_exp_f32_e32 v82, v86
	v_exp_f32_e32 v83, v85
	v_exp_f32_e32 v84, v84
	v_exp_f32_e32 v85, v87
	v_pk_mul_f32 v[70:71], v[70:71], v[80:81]
	v_pk_add_f32 v[82:83], v[82:83], 1.0 op_sel_hi:[1,0]
	v_lshlrev_b64 v[114:115], 12, v[120:121]
	v_pk_add_f32 v[84:85], v[84:85], 1.0 op_sel_hi:[1,0]
	v_lshlrev_b64 v[112:113], 12, v[116:117]
	v_pk_mul_f32 v[86:87], v[82:83], v[84:85]
	v_pk_mul_f32 v[68:69], v[68:69], v[84:85]
	s_mov_b32 s11, 0x358637bd
	v_pk_fma_f32 v[68:69], v[70:71], v[82:83], v[68:69]
	v_rcp_f32_e32 v70, v86
	v_rcp_f32_e32 v71, v87
	s_nop 0
	v_pk_mul_f32 v[74:75], v[68:69], v[70:71]
	v_cvt_pk_bf16_f32 v68, v76, v77
	v_cvt_pk_bf16_f32 v69, v78, v79
	v_cvt_pk_bf16_f32 v70, v72, v73
	v_lshl_add_u64 v[72:73], s[4:5], 0, v[196:197]
	v_lshl_add_u64 v[72:73], v[72:73], 0, v[188:189]
	v_cvt_pk_bf16_f32 v71, v74, v75
	global_store_dwordx4 v[72:73], v[68:71], off
	s_nop 1
	v_lshlrev_b64 v[68:69], 6, v[130:131]
	v_lshl_add_u64 v[68:69], s[44:45], 0, v[68:69]
	v_lshl_add_u64 v[68:69], v[192:193], 0, v[122:123]
	v_lshl_add_u64 v[68:69], v[194:195], 0, v[122:123]
	v_lshlrev_b64 v[68:69], 6, v[124:125]
	v_lshl_add_u64 v[68:69], s[44:45], 0, v[68:69]
	v_lshl_add_u64 v[68:69], v[192:193], 0, v[118:119]
	v_lshl_add_u64 v[68:69], v[194:195], 0, v[118:119]
	v_lshlrev_b64 v[68:69], 6, v[120:121]
	v_lshl_add_u64 v[68:69], s[44:45], 0, v[68:69]
	v_lshl_add_u64 v[68:69], v[192:193], 0, v[114:115]
	v_lshl_add_u64 v[68:69], v[194:195], 0, v[114:115]
	v_lshlrev_b64 v[68:69], 6, v[116:117]
	v_lshl_add_u64 v[68:69], s[44:45], 0, v[68:69]
	v_lshl_add_u64 v[68:69], v[192:193], 0, v[112:113]
	v_and_b32_e32 v117, 0xcf, v130
	global_load_dwordx4 v[72:75], v[68:69], off
	v_lshl_add_u64 v[68:69], v[194:195], 0, v[112:113]
	v_lshl_add_u32 v117, v117, 2, s9
	global_load_dwordx4 v[68:71], v[68:69], off
	v_mov_b32_e32 v117, v229
	s_waitcnt vmcnt(3)
;     __device__ __forceinline__ void operator()(const f32x4 (&acc)[2][2][4][2], const Unit& u, int wr, int wc, int fr, int fq) const {
;     ...
;                 stv[m] = *(const f32x4*)(ST + (size_t)row * 16 + head * 4); yfv[m] = *(const u32x4*)(Y + (size_t)row * 2048 + col0); ybv[m] = *(const u32x4*)(YB + (size_t)row * 2048 + col0); }
; #pragma unroll
;             for (int m = 0; m < 4; ++m) { const int row = row0 + ai * HALF + m * 16; const float r = tab[u.idx * 256 + (row & 255)];
;                 const f32x4 st = stv[m];
;                 const float muf = __builtin_amdgcn_ldexpf(st[0], -9), mub = __builtin_amdgcn_ldexpf(st[2], -9); float eps = 1e-6f; asm volatile("" : "+s"(eps));
;                 const float rf = __builtin_amdgcn_rsqf(fmaxf(__builtin_amdgcn_ldexpf(st[1], -9) - muf * muf, 0.f) + eps), rb = __builtin_amdgcn_rsqf(fmaxf(__builtin_amdgcn_ldexpf(st[3], -9) - mub * mub, 0.f) + eps);
;                 const float cf = rf * r, cb = rb * r, df = -muf * cf, db = -mub * cb, kr = -1.4426950409f * r;
;                 const u32x4 yfw = yfv[m], ybw = ybv[m];
;                 float o[8];
; #pragma unroll
;                 for (int n = 0; n < 2; ++n)
; #pragma unroll
;                     for (int e = 0; e < 4; e += 2) { const int q = n * 4 + e; const unsigned wf = yfw[q >> 1], wb = ybw[q >> 1];
;                         const f32x2 yf2 = {__builtin_bit_cast(float, wf << 16), __builtin_bit_cast(float, wf & 0xffff0000u)}, yb2 = {__builtin_bit_cast(float, wb << 16), __builtin_bit_cast(float, wb & 0xffff0000u)};
;                         const f32x2 af = {acc[ai][0][m][n][e], acc[ai][0][m][n][e + 1]}, ab = {acc[ai][1][m][n][e], acc[ai][1][m][n][e + 1]};
;                         const f32x2 nf = yf2 * cf + df, nb = yb2 * cb + db;
;                         const f32x2 xf = __builtin_elementwise_min(af * kr, (f32x2){60.f, 60.f}), xb = __builtin_elementwise_min(ab * kr, (f32x2){60.f, 60.f});
;                         const f32x2 pf = (f32x2){__builtin_amdgcn_exp2f(xf[0]), __builtin_amdgcn_exp2f(xf[1])} + 1.0f, pb = (f32x2){__builtin_amdgcn_exp2f(xb[0]), __builtin_amdgcn_exp2f(xb[1])} + 1.0f;
;                         const f32x2 den = pf * pb, num = (af * nf) * pb + (ab * nb) * pf;
;                         const f32x2 res = num * (f32x2){__builtin_amdgcn_rcpf(den[0]), __builtin_amdgcn_rcpf(den[1])};
;                         o[q] = res[0]; o[q + 1] = res[1]; }
	v_mov_b64_e32 v[126:127], v[168:169]
	v_mov_b64_e32 v[128:129], v[170:171]
	v_mov_b64_e32 v[108:109], v[172:173]
	v_mov_b64_e32 v[110:111], v[174:175]
	v_mov_b64_e32 v[104:105], v[200:201]
	v_mov_b64_e32 v[106:107], v[202:203]
	v_mov_b64_e32 v[100:101], v[208:209]
	v_mov_b64_e32 v[102:103], v[210:211]
	v_mov_b64_e32 v[96:97], v[156:157]
	v_mov_b64_e32 v[98:99], v[158:159]
	v_mov_b64_e32 v[92:93], v[160:161]
	v_mov_b64_e32 v[94:95], v[162:163]
	v_mov_b64_e32 v[88:89], v[164:165]
	v_mov_b64_e32 v[90:91], v[166:167]
	v_mov_b64_e32 v[84:85], v[148:149]
	v_mov_b64_e32 v[86:87], v[150:151]
	v_mov_b64_e32 v[80:81], v[212:213]
	v_mov_b64_e32 v[82:83], v[214:215]
	v_mov_b64_e32 v[76:77], v[152:153]
	v_mov_b64_e32 v[78:79], v[154:155]
	s_waitcnt vmcnt(11)
	v_ldexp_f32 v121, v126, -9
	v_ldexp_f32 v126, v127, -9
	v_ldexp_f32 v125, v128, -9
	v_fma_f32 v126, -v121, v121, v126
	v_ldexp_f32 v127, v129, -9
	v_max_f32_e32 v126, 0, v126
	v_fma_f32 v127, -v125, v125, v127
	v_add_f32_e32 v126, s11, v126
	v_max_f32_e32 v127, 0, v127
	v_rsq_f32_e32 v126, v126
	v_add_f32_e32 v127, s11, v127
	v_rsq_f32_e32 v127, v127
	s_waitcnt vmcnt(10)
	v_lshlrev_b32_e32 v136, 16, v108
	s_waitcnt lgkmcnt(0)
	v_mul_f32_e32 v128, v117, v126
	v_mul_f32_e32 v126, 0xbfb8aa3b, v117
	v_pk_mul_f32 v[140:141], v[64:65], v[126:127] op_sel_hi:[1,0]
	v_and_b32_e32 v137, 0xffff0000, v108
	s_waitcnt vmcnt(9)
	v_lshlrev_b32_e32 v138, 16, v104
	v_and_b32_e32 v139, 0xffff0000, v104
	v_min_f32_e32 v104, 0x42700000, v141
	v_min_f32_e32 v108, 0x42700000, v140
	v_pk_mul_f32 v[140:141], v[60:61], v[126:127] op_sel_hi:[1,0]
	v_mul_f32_e32 v130, v117, v127
	v_mul_f32_e64 v132, v128, -v121
	v_min_f32_e32 v117, 0x42700000, v141
	v_min_f32_e32 v121, 0x42700000, v140
	v_exp_f32_e32 v140, v108
	v_exp_f32_e32 v141, v104
	v_exp_f32_e32 v142, v121
	v_exp_f32_e32 v143, v117
	v_mul_f32_e64 v134, v130, -v125
	v_pk_fma_f32 v[136:137], v[128:129], v[136:137], v[132:133] op_sel_hi:[0,1,0]
	v_pk_fma_f32 v[138:139], v[130:131], v[138:139], v[134:135] op_sel_hi:[0,1,0]
	v_pk_add_f32 v[140:141], v[140:141], 1.0 op_sel_hi:[1,0]
	v_pk_add_f32 v[142:143], v[142:143], 1.0 op_sel_hi:[1,0]
	v_pk_mul_f32 v[64:65], v[64:65], v[136:137]
	v_pk_mul_f32 v[144:145], v[140:141], v[142:143]
	v_pk_mul_f32 v[64:65], v[64:65], v[142:143]
	v_pk_mul_f32 v[60:61], v[60:61], v[138:139]
	v_lshlrev_b32_e32 v104, 16, v105
	v_pk_fma_f32 v[60:61], v[60:61], v[140:141], v[64:65]
	v_rcp_f32_e32 v64, v144
	v_rcp_f32_e32 v65, v145
	v_and_b32_e32 v105, 0xffff0000, v105
	v_pk_fma_f32 v[104:105], v[130:131], v[104:105], v[134:135] op_sel_hi:[0,1,0]
	s_mov_b32 s11, 0x358637bd
	v_pk_mul_f32 v[60:61], v[60:61], v[64:65]
	v_lshlrev_b32_e32 v64, 16, v109
	v_and_b32_e32 v65, 0xffff0000, v109
	v_pk_mul_f32 v[108:109], v[66:67], v[126:127] op_sel_hi:[1,0]
	v_pk_fma_f32 v[64:65], v[128:129], v[64:65], v[132:133] op_sel_hi:[0,1,0]
	v_min_f32_e32 v117, 0x42700000, v109
	v_min_f32_e32 v121, 0x42700000, v108
	v_pk_mul_f32 v[108:109], v[62:63], v[126:127] op_sel_hi:[1,0]
	v_pk_mul_f32 v[64:65], v[66:67], v[64:65]
	v_min_f32_e32 v125, 0x42700000, v109
	v_min_f32_e32 v127, 0x42700000, v108
	v_exp_f32_e32 v108, v121
	v_exp_f32_e32 v109, v117
	v_exp_f32_e32 v136, v127
	v_exp_f32_e32 v137, v125
	v_pk_mul_f32 v[62:63], v[62:63], v[104:105]
	v_pk_add_f32 v[108:109], v[108:109], 1.0 op_sel_hi:[1,0]
	v_pk_mul_f32 v[104:105], v[56:57], v[126:127] op_sel_hi:[1,0]
	v_pk_add_f32 v[136:137], v[136:137], 1.0 op_sel_hi:[1,0]
	v_lshlrev_b32_e32 v66, 16, v106
	v_pk_mul_f32 v[138:139], v[108:109], v[136:137]
	v_pk_mul_f32 v[64:65], v[64:65], v[136:137]
	v_and_b32_e32 v67, 0xffff0000, v106
	v_pk_fma_f32 v[62:63], v[62:63], v[108:109], v[64:65]
	v_rcp_f32_e32 v64, v138
	v_rcp_f32_e32 v65, v139
	v_min_f32_e32 v106, 0x42700000, v105
	v_min_f32_e32 v108, 0x42700000, v104
	v_pk_mul_f32 v[104:105], v[52:53], v[126:127] op_sel_hi:[1,0]
	v_pk_mul_f32 v[62:63], v[62:63], v[64:65]
	v_lshlrev_b32_e32 v64, 16, v110
	v_and_b32_e32 v65, 0xffff0000, v110
	v_min_f32_e32 v109, 0x42700000, v105
	v_min_f32_e32 v110, 0x42700000, v104
	v_exp_f32_e32 v104, v108
	v_exp_f32_e32 v105, v106
	v_exp_f32_e32 v108, v110
	v_exp_f32_e32 v109, v109
	v_pk_fma_f32 v[64:65], v[128:129], v[64:65], v[132:133] op_sel_hi:[0,1,0]
	v_pk_fma_f32 v[66:67], v[130:131], v[66:67], v[134:135] op_sel_hi:[0,1,0]
	v_pk_add_f32 v[104:105], v[104:105], 1.0 op_sel_hi:[1,0]
	v_pk_add_f32 v[108:109], v[108:109], 1.0 op_sel_hi:[1,0]
	v_pk_mul_f32 v[56:57], v[56:57], v[64:65]
	v_pk_mul_f32 v[136:137], v[104:105], v[108:109]
	v_pk_mul_f32 v[56:57], v[56:57], v[108:109]
	v_pk_mul_f32 v[52:53], v[52:53], v[66:67]
	v_pk_mul_f32 v[66:67], v[58:59], v[126:127] op_sel_hi:[1,0]
	v_pk_fma_f32 v[52:53], v[52:53], v[104:105], v[56:57]
	v_rcp_f32_e32 v56, v136
	v_rcp_f32_e32 v57, v137
	v_min_f32_e32 v104, 0x42700000, v67
	v_min_f32_e32 v105, 0x42700000, v66
	v_pk_mul_f32 v[66:67], v[54:55], v[126:127] op_sel_hi:[1,0]
	v_lshlrev_b32_e32 v64, 16, v107
	v_and_b32_e32 v65, 0xffff0000, v107
	v_min_f32_e32 v106, 0x42700000, v67
	v_min_f32_e32 v107, 0x42700000, v66
	v_exp_f32_e32 v66, v105
	v_exp_f32_e32 v67, v104
	v_exp_f32_e32 v104, v107
	v_exp_f32_e32 v105, v106
	v_pk_mul_f32 v[56:57], v[52:53], v[56:57]
	v_lshlrev_b32_e32 v52, 16, v111
	v_and_b32_e32 v53, 0xffff0000, v111
	v_pk_fma_f32 v[52:53], v[128:129], v[52:53], v[132:133] op_sel_hi:[0,1,0]
	v_pk_fma_f32 v[64:65], v[130:131], v[64:65], v[134:135] op_sel_hi:[0,1,0]
	v_pk_add_f32 v[66:67], v[66:67], 1.0 op_sel_hi:[1,0]
	v_pk_add_f32 v[104:105], v[104:105], 1.0 op_sel_hi:[1,0]
	v_pk_mul_f32 v[52:53], v[58:59], v[52:53]
	v_pk_mul_f32 v[106:107], v[66:67], v[104:105]
	v_pk_mul_f32 v[52:53], v[52:53], v[104:105]
	v_pk_mul_f32 v[54:55], v[54:55], v[64:65]
	s_waitcnt vmcnt(6)
;     __device__ __forceinline__ void operator()(const f32x4 (&acc)[2][2][4][2], const Unit& u, int wr, int wc, int fr, int fq) const {
;     ...
;             for (int m = 0; m < 4; ++m) { const int row = row0 + ai * HALF + m * 16; const float r = tab[u.idx * 256 + (row & 255)];
;                 const f32x4 st = stv[m];
;                 const float muf = __builtin_amdgcn_ldexpf(st[0], -9), mub = __builtin_amdgcn_ldexpf(st[2], -9); float eps = 1e-6f; asm volatile("" : "+s"(eps));
;                 const float rf = __builtin_amdgcn_rsqf(fmaxf(__builtin_amdgcn_ldexpf(st[1], -9) - muf * muf, 0.f) + eps), rb = __builtin_amdgcn_rsqf(fmaxf(__builtin_amdgcn_ldexpf(st[3], -9) - mub * mub, 0.f) + eps);
;                 const float cf = rf * r, cb = rb * r, df = -muf * cf, db = -mub * cb, kr = -1.4426950409f * r;
;                 const u32x4 yfw = yfv[m], ybw = ybv[m];
;                 float o[8];
; #pragma unroll
;                 for (int n = 0; n < 2; ++n)
; #pragma unroll
;                     for (int e = 0; e < 4; e += 2) { const int q = n * 4 + e; const unsigned wf = yfw[q >> 1], wb = ybw[q >> 1];
;                         const f32x2 yf2 = {__builtin_bit_cast(float, wf << 16), __builtin_bit_cast(float, wf & 0xffff0000u)}, yb2 = {__builtin_bit_cast(float, wb << 16), __builtin_bit_cast(float, wb & 0xffff0000u)};
;                         const f32x2 af = {acc[ai][0][m][n][e], acc[ai][0][m][n][e + 1]}, ab = {acc[ai][1][m][n][e], acc[ai][1][m][n][e + 1]};
;                         const f32x2 nf = yf2 * cf + df, nb = yb2 * cb + db;
;                         const f32x2 xf = __builtin_elementwise_min(af * kr, (f32x2){60.f, 60.f}), xb = __builtin_elementwise_min(ab * kr, (f32x2){60.f, 60.f});
;                         const f32x2 pf = (f32x2){__builtin_amdgcn_exp2f(xf[0]), __builtin_amdgcn_exp2f(xf[1])} + 1.0f, pb = (f32x2){__builtin_amdgcn_exp2f(xb[0]), __builtin_amdgcn_exp2f(xb[1])} + 1.0f;
;                         const f32x2 den = pf * pb, num = (af * nf) * pb + (ab * nb) * pf;
;                         const f32x2 res = num * (f32x2){__builtin_amdgcn_rcpf(den[0]), __builtin_amdgcn_rcpf(den[1])};
;                         o[q] = res[0]; o[q + 1] = res[1]; }
;                 u32x4 w; w.x = cvt_pk_bf16(o[0], o[1]); w.y = cvt_pk_bf16(o[2], o[3]); w.z = cvt_pk_bf16(o[4], o[5]); w.w = cvt_pk_bf16(o[6], o[7]);
	v_lshlrev_b32_e32 v64, 16, v92
	v_pk_fma_f32 v[52:53], v[54:55], v[66:67], v[52:53]
	v_rcp_f32_e32 v54, v106
	v_rcp_f32_e32 v55, v107
	v_and_b32_e32 v65, 0xffff0000, v92
	v_pk_mul_f32 v[58:59], v[52:53], v[54:55]
	v_cvt_pk_bf16_f32 v52, v60, v61
	v_cvt_pk_bf16_f32 v53, v62, v63
	v_cvt_pk_bf16_f32 v54, v56, v57
	v_lshl_add_u64 v[56:57], s[4:5], 0, v[122:123]
	v_cvt_pk_bf16_f32 v55, v58, v59
	v_lshl_add_u64 v[56:57], v[56:57], 0, v[188:189]
	global_store_dwordx4 v[56:57], v[52:55], off
	v_ldexp_f32 v56, v103, -9
	v_lshlrev_b32_e32 v62, 16, v96
	v_ldexp_f32 v53, v100, -9
	v_ldexp_f32 v55, v102, -9
	v_ldexp_f32 v54, v101, -9
	v_and_b32_e32 v52, 0xdf, v124
	v_fma_f32 v54, -v53, v53, v54
	v_fma_f32 v56, -v55, v55, v56
	v_lshl_add_u32 v52, v52, 2, s9
	v_max_f32_e32 v54, 0, v54
	v_max_f32_e32 v56, 0, v56
	v_mov_b32_e32 v52, v230
	v_and_b32_e32 v63, 0xffff0000, v96
	v_add_f32_e32 v54, s11, v54
	v_add_f32_e32 v56, s11, v56
	v_rsq_f32_e32 v54, v54
	v_rsq_f32_e32 v56, v56
	s_mov_b32 s11, 0x358637bd
	s_waitcnt lgkmcnt(0)
	v_mul_f32_e32 v54, v52, v54
	v_mul_f32_e32 v56, v52, v56
	v_mul_f32_e32 v52, 0xbfb8aa3b, v52
	v_pk_mul_f32 v[66:67], v[48:49], v[52:53] op_sel_hi:[1,0]
	v_mul_f32_e64 v58, v54, -v53
	v_min_f32_e32 v53, 0x42700000, v67
	v_mul_f32_e64 v60, v56, -v55
	v_pk_fma_f32 v[62:63], v[54:55], v[62:63], v[58:59] op_sel_hi:[0,1,0]
	v_min_f32_e32 v55, 0x42700000, v66
	v_pk_mul_f32 v[66:67], v[44:45], v[52:53] op_sel_hi:[1,0]
	v_pk_fma_f32 v[64:65], v[56:57], v[64:65], v[60:61] op_sel_hi:[0,1,0]
	v_min_f32_e32 v57, 0x42700000, v67
	v_min_f32_e32 v59, 0x42700000, v66
	v_exp_f32_e32 v66, v55
	v_exp_f32_e32 v67, v53
	v_exp_f32_e32 v100, v59
	v_exp_f32_e32 v101, v57
	v_pk_mul_f32 v[48:49], v[48:49], v[62:63]
	v_pk_add_f32 v[66:67], v[66:67], 1.0 op_sel_hi:[1,0]
	v_pk_mul_f32 v[44:45], v[44:45], v[64:65]
	v_pk_add_f32 v[100:101], v[100:101], 1.0 op_sel_hi:[1,0]
	v_pk_mul_f32 v[64:65], v[50:51], v[52:53] op_sel_hi:[1,0]
	v_pk_mul_f32 v[102:103], v[66:67], v[100:101]
	v_pk_mul_f32 v[48:49], v[48:49], v[100:101]
	v_min_f32_e32 v53, 0x42700000, v65
	v_pk_fma_f32 v[44:45], v[44:45], v[66:67], v[48:49]
	v_rcp_f32_e32 v48, v102
	v_rcp_f32_e32 v49, v103
	v_lshlrev_b32_e32 v62, 16, v93
	v_and_b32_e32 v63, 0xffff0000, v93
	v_pk_fma_f32 v[62:63], v[56:57], v[62:63], v[60:61] op_sel_hi:[0,1,0]
	v_pk_mul_f32 v[44:45], v[44:45], v[48:49]
	v_lshlrev_b32_e32 v48, 16, v97
	v_and_b32_e32 v49, 0xffff0000, v97
	v_pk_fma_f32 v[48:49], v[54:55], v[48:49], v[58:59] op_sel_hi:[0,1,0]
	v_min_f32_e32 v55, 0x42700000, v64
	v_pk_mul_f32 v[64:65], v[46:47], v[52:53] op_sel_hi:[1,0]
	v_pk_mul_f32 v[48:49], v[50:51], v[48:49]
	v_min_f32_e32 v57, 0x42700000, v65
	v_min_f32_e32 v59, 0x42700000, v64
	v_exp_f32_e32 v64, v55
	v_exp_f32_e32 v65, v53
	v_exp_f32_e32 v66, v59
	v_exp_f32_e32 v67, v57
	v_pk_mul_f32 v[46:47], v[46:47], v[62:63]
	v_pk_add_f32 v[64:65], v[64:65], 1.0 op_sel_hi:[1,0]
	v_pk_mul_f32 v[62:63], v[40:41], v[52:53] op_sel_hi:[1,0]
	v_pk_add_f32 v[66:67], v[66:67], 1.0 op_sel_hi:[1,0]
	v_min_f32_e32 v53, 0x42700000, v63
	v_pk_mul_f32 v[92:93], v[64:65], v[66:67]
	v_pk_mul_f32 v[48:49], v[48:49], v[66:67]
	v_lshlrev_b32_e32 v50, 16, v94
	v_pk_fma_f32 v[46:47], v[46:47], v[64:65], v[48:49]
	v_rcp_f32_e32 v48, v92
	v_rcp_f32_e32 v49, v93
	v_and_b32_e32 v51, 0xffff0000, v94
	v_pk_fma_f32 v[50:51], v[56:57], v[50:51], v[60:61] op_sel_hi:[0,1,0]
	v_pk_mul_f32 v[46:47], v[46:47], v[48:49]
	v_lshlrev_b32_e32 v48, 16, v98
	v_and_b32_e32 v49, 0xffff0000, v98
	v_pk_fma_f32 v[48:49], v[54:55], v[48:49], v[58:59] op_sel_hi:[0,1,0]
	v_min_f32_e32 v55, 0x42700000, v62
	v_pk_mul_f32 v[62:63], v[36:37], v[52:53] op_sel_hi:[1,0]
	v_pk_mul_f32 v[40:41], v[40:41], v[48:49]
	v_min_f32_e32 v57, 0x42700000, v63
	v_min_f32_e32 v59, 0x42700000, v62
	v_exp_f32_e32 v62, v55
	v_exp_f32_e32 v63, v53
	v_exp_f32_e32 v64, v59
	v_exp_f32_e32 v65, v57
	v_pk_mul_f32 v[36:37], v[36:37], v[50:51]
	v_pk_add_f32 v[62:63], v[62:63], 1.0 op_sel_hi:[1,0]
	v_pk_mul_f32 v[50:51], v[42:43], v[52:53] op_sel_hi:[1,0]
	v_pk_add_f32 v[64:65], v[64:65], 1.0 op_sel_hi:[1,0]
	v_min_f32_e32 v53, 0x42700000, v51
	v_pk_mul_f32 v[66:67], v[62:63], v[64:65]
	v_pk_mul_f32 v[40:41], v[40:41], v[64:65]
	v_lshlrev_b32_e32 v48, 16, v95
	v_pk_fma_f32 v[36:37], v[36:37], v[62:63], v[40:41]
	v_rcp_f32_e32 v40, v66
	v_rcp_f32_e32 v41, v67
	v_and_b32_e32 v49, 0xffff0000, v95
	v_pk_fma_f32 v[48:49], v[56:57], v[48:49], v[60:61] op_sel_hi:[0,1,0]
	v_pk_mul_f32 v[40:41], v[36:37], v[40:41]
	v_lshlrev_b32_e32 v36, 16, v99
	v_and_b32_e32 v37, 0xffff0000, v99
	v_pk_fma_f32 v[36:37], v[54:55], v[36:37], v[58:59] op_sel_hi:[0,1,0]
	v_min_f32_e32 v54, 0x42700000, v50
	v_pk_mul_f32 v[50:51], v[38:39], v[52:53] op_sel_hi:[1,0]
	v_pk_mul_f32 v[36:37], v[42:43], v[36:37]
	v_min_f32_e32 v55, 0x42700000, v51
	v_min_f32_e32 v52, 0x42700000, v50
	v_exp_f32_e32 v50, v54
	v_exp_f32_e32 v51, v53
	v_exp_f32_e32 v52, v52
	v_exp_f32_e32 v53, v55
	v_pk_mul_f32 v[38:39], v[38:39], v[48:49]
	v_pk_add_f32 v[50:51], v[50:51], 1.0 op_sel_hi:[1,0]
	s_waitcnt vmcnt(4)
	v_lshlrev_b32_e32 v48, 16, v80
	v_pk_add_f32 v[52:53], v[52:53], 1.0 op_sel_hi:[1,0]
	v_and_b32_e32 v49, 0xffff0000, v80
	v_pk_mul_f32 v[54:55], v[50:51], v[52:53]
	v_pk_mul_f32 v[36:37], v[36:37], v[52:53]
	s_nop 0
	v_pk_fma_f32 v[36:37], v[38:39], v[50:51], v[36:37]
	v_rcp_f32_e32 v38, v54
	v_rcp_f32_e32 v39, v55
	s_nop 0
	v_pk_mul_f32 v[42:43], v[36:37], v[38:39]
	v_cvt_pk_bf16_f32 v36, v44, v45
	v_cvt_pk_bf16_f32 v37, v46, v47
	v_cvt_pk_bf16_f32 v38, v40, v41
	v_lshl_add_u64 v[40:41], s[4:5], 0, v[118:119]
	v_cvt_pk_bf16_f32 v39, v42, v43
	v_lshl_add_u64 v[40:41], v[40:41], 0, v[188:189]
	global_store_dwordx4 v[40:41], v[36:39], off
	v_ldexp_f32 v40, v91, -9
	v_lshlrev_b32_e32 v46, 16, v84
	v_ldexp_f32 v37, v88, -9
	v_ldexp_f32 v39, v90, -9
	v_ldexp_f32 v38, v89, -9
	v_and_b32_e32 v36, 0xef, v120
	v_fma_f32 v38, -v37, v37, v38
	v_fma_f32 v40, -v39, v39, v40
	v_lshl_add_u32 v36, v36, 2, s9
	v_max_f32_e32 v38, 0, v38
	v_max_f32_e32 v40, 0, v40
	v_mov_b32_e32 v36, v231
	v_and_b32_e32 v47, 0xffff0000, v84
	v_add_f32_e32 v38, s11, v38
	v_add_f32_e32 v40, s11, v40
	v_rsq_f32_e32 v38, v38
	v_rsq_f32_e32 v40, v40
	s_waitcnt lgkmcnt(0)
;     __device__ __forceinline__ void operator()(const f32x4 (&acc)[2][2][4][2], const Unit& u, int wr, int wc, int fr, int fq) const {
;     ...
;             for (int m = 0; m < 4; ++m) { const int row = row0 + ai * HALF + m * 16; const float r = tab[u.idx * 256 + (row & 255)];
;                 const f32x4 st = stv[m];
;                 const float muf = __builtin_amdgcn_ldexpf(st[0], -9), mub = __builtin_amdgcn_ldexpf(st[2], -9); float eps = 1e-6f; asm volatile("" : "+s"(eps));
;                 const float rf = __builtin_amdgcn_rsqf(fmaxf(__builtin_amdgcn_ldexpf(st[1], -9) - muf * muf, 0.f) + eps), rb = __builtin_amdgcn_rsqf(fmaxf(__builtin_amdgcn_ldexpf(st[3], -9) - mub * mub, 0.f) + eps);
;                 const float cf = rf * r, cb = rb * r, df = -muf * cf, db = -mub * cb, kr = -1.4426950409f * r;
;                 const u32x4 yfw = yfv[m], ybw = ybv[m];
;                 float o[8];
; #pragma unroll
;                 for (int n = 0; n < 2; ++n)
; #pragma unroll
;                     for (int e = 0; e < 4; e += 2) { const int q = n * 4 + e; const unsigned wf = yfw[q >> 1], wb = ybw[q >> 1];
;                         const f32x2 yf2 = {__builtin_bit_cast(float, wf << 16), __builtin_bit_cast(float, wf & 0xffff0000u)}, yb2 = {__builtin_bit_cast(float, wb << 16), __builtin_bit_cast(float, wb & 0xffff0000u)};
;                         const f32x2 af = {acc[ai][0][m][n][e], acc[ai][0][m][n][e + 1]}, ab = {acc[ai][1][m][n][e], acc[ai][1][m][n][e + 1]};
;                         const f32x2 nf = yf2 * cf + df, nb = yb2 * cb + db;
;                         const f32x2 xf = __builtin_elementwise_min(af * kr, (f32x2){60.f, 60.f}), xb = __builtin_elementwise_min(ab * kr, (f32x2){60.f, 60.f});
;                         const f32x2 pf = (f32x2){__builtin_amdgcn_exp2f(xf[0]), __builtin_amdgcn_exp2f(xf[1])} + 1.0f, pb = (f32x2){__builtin_amdgcn_exp2f(xb[0]), __builtin_amdgcn_exp2f(xb[1])} + 1.0f;
;                         const f32x2 den = pf * pb, num = (af * nf) * pb + (ab * nb) * pf;
;                         const f32x2 res = num * (f32x2){__builtin_amdgcn_rcpf(den[0]), __builtin_amdgcn_rcpf(den[1])};
;                         o[q] = res[0]; o[q + 1] = res[1]; }
	v_mul_f32_e32 v38, v36, v38
	v_mul_f32_e32 v40, v36, v40
	v_mul_f32_e32 v36, 0xbfb8aa3b, v36
	v_pk_mul_f32 v[50:51], v[32:33], v[36:37] op_sel_hi:[1,0]
	v_mul_f32_e64 v42, v38, -v37
	v_min_f32_e32 v37, 0x42700000, v51
	v_mul_f32_e64 v44, v40, -v39
	v_pk_fma_f32 v[46:47], v[38:39], v[46:47], v[42:43] op_sel_hi:[0,1,0]
	v_min_f32_e32 v39, 0x42700000, v50
	v_pk_mul_f32 v[50:51], v[28:29], v[36:37] op_sel_hi:[1,0]
	v_pk_fma_f32 v[48:49], v[40:41], v[48:49], v[44:45] op_sel_hi:[0,1,0]
	v_min_f32_e32 v41, 0x42700000, v51
	v_min_f32_e32 v43, 0x42700000, v50
	v_exp_f32_e32 v50, v39
	v_exp_f32_e32 v51, v37
	v_exp_f32_e32 v52, v43
	v_exp_f32_e32 v53, v41
	v_pk_mul_f32 v[32:33], v[32:33], v[46:47]
	v_pk_add_f32 v[50:51], v[50:51], 1.0 op_sel_hi:[1,0]
	v_pk_mul_f32 v[28:29], v[28:29], v[48:49]
	v_pk_add_f32 v[52:53], v[52:53], 1.0 op_sel_hi:[1,0]
	v_pk_mul_f32 v[48:49], v[34:35], v[36:37] op_sel_hi:[1,0]
	v_pk_mul_f32 v[54:55], v[50:51], v[52:53]
	v_pk_mul_f32 v[32:33], v[32:33], v[52:53]
	v_min_f32_e32 v37, 0x42700000, v49
	v_pk_fma_f32 v[28:29], v[28:29], v[50:51], v[32:33]
	v_rcp_f32_e32 v32, v54
	v_rcp_f32_e32 v33, v55
	v_lshlrev_b32_e32 v46, 16, v81
	v_and_b32_e32 v47, 0xffff0000, v81
	v_pk_fma_f32 v[46:47], v[40:41], v[46:47], v[44:45] op_sel_hi:[0,1,0]
	v_pk_mul_f32 v[28:29], v[28:29], v[32:33]
	v_lshlrev_b32_e32 v32, 16, v85
	v_and_b32_e32 v33, 0xffff0000, v85
	v_pk_fma_f32 v[32:33], v[38:39], v[32:33], v[42:43] op_sel_hi:[0,1,0]
	v_min_f32_e32 v39, 0x42700000, v48
	v_pk_mul_f32 v[48:49], v[30:31], v[36:37] op_sel_hi:[1,0]
	v_pk_mul_f32 v[32:33], v[34:35], v[32:33]
	v_min_f32_e32 v41, 0x42700000, v49
	v_min_f32_e32 v43, 0x42700000, v48
	v_exp_f32_e32 v48, v39
	v_exp_f32_e32 v49, v37
	v_exp_f32_e32 v50, v43
	v_exp_f32_e32 v51, v41
	v_pk_mul_f32 v[30:31], v[30:31], v[46:47]
	v_pk_add_f32 v[48:49], v[48:49], 1.0 op_sel_hi:[1,0]
	v_pk_mul_f32 v[46:47], v[24:25], v[36:37] op_sel_hi:[1,0]
	v_pk_add_f32 v[50:51], v[50:51], 1.0 op_sel_hi:[1,0]
	v_min_f32_e32 v37, 0x42700000, v47
	v_pk_mul_f32 v[52:53], v[48:49], v[50:51]
	v_pk_mul_f32 v[32:33], v[32:33], v[50:51]
	v_lshlrev_b32_e32 v34, 16, v82
	v_pk_fma_f32 v[30:31], v[30:31], v[48:49], v[32:33]
	v_rcp_f32_e32 v32, v52
	v_rcp_f32_e32 v33, v53
	v_and_b32_e32 v35, 0xffff0000, v82
	v_pk_fma_f32 v[34:35], v[40:41], v[34:35], v[44:45] op_sel_hi:[0,1,0]
	v_pk_mul_f32 v[30:31], v[30:31], v[32:33]
	v_lshlrev_b32_e32 v32, 16, v86
	v_and_b32_e32 v33, 0xffff0000, v86
	v_pk_fma_f32 v[32:33], v[38:39], v[32:33], v[42:43] op_sel_hi:[0,1,0]
	v_min_f32_e32 v39, 0x42700000, v46
	v_pk_mul_f32 v[46:47], v[20:21], v[36:37] op_sel_hi:[1,0]
	v_pk_mul_f32 v[24:25], v[24:25], v[32:33]
	v_min_f32_e32 v41, 0x42700000, v47
	v_min_f32_e32 v43, 0x42700000, v46
	v_exp_f32_e32 v46, v39
	v_exp_f32_e32 v47, v37
	v_exp_f32_e32 v48, v43
	v_exp_f32_e32 v49, v41
	v_pk_mul_f32 v[20:21], v[20:21], v[34:35]
	v_pk_add_f32 v[46:47], v[46:47], 1.0 op_sel_hi:[1,0]
	v_pk_mul_f32 v[34:35], v[26:27], v[36:37] op_sel_hi:[1,0]
	v_pk_add_f32 v[48:49], v[48:49], 1.0 op_sel_hi:[1,0]
	v_min_f32_e32 v37, 0x42700000, v35
	v_pk_mul_f32 v[50:51], v[46:47], v[48:49]
	v_pk_mul_f32 v[24:25], v[24:25], v[48:49]
	v_lshlrev_b32_e32 v32, 16, v83
	v_pk_fma_f32 v[20:21], v[20:21], v[46:47], v[24:25]
	v_rcp_f32_e32 v24, v50
	v_rcp_f32_e32 v25, v51
	v_and_b32_e32 v33, 0xffff0000, v83
	v_pk_fma_f32 v[32:33], v[40:41], v[32:33], v[44:45] op_sel_hi:[0,1,0]
	v_pk_mul_f32 v[24:25], v[20:21], v[24:25]
	v_lshlrev_b32_e32 v20, 16, v87
	v_and_b32_e32 v21, 0xffff0000, v87
	v_pk_fma_f32 v[20:21], v[38:39], v[20:21], v[42:43] op_sel_hi:[0,1,0]
	v_min_f32_e32 v38, 0x42700000, v34
	v_pk_mul_f32 v[34:35], v[22:23], v[36:37] op_sel_hi:[1,0]
	v_pk_mul_f32 v[20:21], v[26:27], v[20:21]
	v_min_f32_e32 v39, 0x42700000, v35
	v_min_f32_e32 v36, 0x42700000, v34
	v_exp_f32_e32 v34, v38
	v_exp_f32_e32 v35, v37
	v_exp_f32_e32 v36, v36
	v_exp_f32_e32 v37, v39
	v_pk_mul_f32 v[22:23], v[22:23], v[32:33]
	v_pk_add_f32 v[34:35], v[34:35], 1.0 op_sel_hi:[1,0]
	s_waitcnt vmcnt(2)
	v_lshlrev_b32_e32 v32, 16, v68
	v_pk_add_f32 v[36:37], v[36:37], 1.0 op_sel_hi:[1,0]
	v_and_b32_e32 v33, 0xffff0000, v68
	v_pk_mul_f32 v[38:39], v[34:35], v[36:37]
	v_pk_mul_f32 v[20:21], v[20:21], v[36:37]
	s_nop 0
	v_pk_fma_f32 v[20:21], v[22:23], v[34:35], v[20:21]
	v_rcp_f32_e32 v22, v38
	v_rcp_f32_e32 v23, v39
	s_nop 0
	v_pk_mul_f32 v[26:27], v[20:21], v[22:23]
	v_cvt_pk_bf16_f32 v20, v28, v29
	v_cvt_pk_bf16_f32 v21, v30, v31
	v_cvt_pk_bf16_f32 v22, v24, v25
	v_lshl_add_u64 v[24:25], s[4:5], 0, v[114:115]
	v_cvt_pk_bf16_f32 v23, v26, v27
	v_lshl_add_u64 v[24:25], v[24:25], 0, v[188:189]
	global_store_dwordx4 v[24:25], v[20:23], off
	v_ldexp_f32 v24, v79, -9
	v_lshlrev_b32_e32 v30, 16, v72
	v_ldexp_f32 v21, v76, -9
	v_ldexp_f32 v23, v78, -9
	v_ldexp_f32 v22, v77, -9
	v_and_b32_e32 v20, 0xff, v116
	v_fma_f32 v22, -v21, v21, v22
	v_fma_f32 v24, -v23, v23, v24
	v_lshl_add_u32 v20, v20, 2, s9
	s_mov_b32 s9, 0x358637bd
	v_max_f32_e32 v22, 0, v22
	v_max_f32_e32 v24, 0, v24
	v_mov_b32_e32 v20, v232
	v_and_b32_e32 v31, 0xffff0000, v72
	v_add_f32_e32 v22, s9, v22
	v_add_f32_e32 v24, s9, v24
	v_rsq_f32_e32 v22, v22
	v_rsq_f32_e32 v24, v24
	s_waitcnt lgkmcnt(0)
;     __device__ __forceinline__ void operator()(const f32x4 (&acc)[2][2][4][2], const Unit& u, int wr, int wc, int fr, int fq) const {
;     ...
;             for (int m = 0; m < 4; ++m) { const int row = row0 + ai * HALF + m * 16; const float r = tab[u.idx * 256 + (row & 255)];
;                 const f32x4 st = stv[m];
;                 const float muf = __builtin_amdgcn_ldexpf(st[0], -9), mub = __builtin_amdgcn_ldexpf(st[2], -9); float eps = 1e-6f; asm volatile("" : "+s"(eps));
;                 const float rf = __builtin_amdgcn_rsqf(fmaxf(__builtin_amdgcn_ldexpf(st[1], -9) - muf * muf, 0.f) + eps), rb = __builtin_amdgcn_rsqf(fmaxf(__builtin_amdgcn_ldexpf(st[3], -9) - mub * mub, 0.f) + eps);
;                 const float cf = rf * r, cb = rb * r, df = -muf * cf, db = -mub * cb, kr = -1.4426950409f * r;
;                 const u32x4 yfw = yfv[m], ybw = ybv[m];
;                 float o[8];
; #pragma unroll
;                 for (int n = 0; n < 2; ++n)
; #pragma unroll
;                     for (int e = 0; e < 4; e += 2) { const int q = n * 4 + e; const unsigned wf = yfw[q >> 1], wb = ybw[q >> 1];
;                         const f32x2 yf2 = {__builtin_bit_cast(float, wf << 16), __builtin_bit_cast(float, wf & 0xffff0000u)}, yb2 = {__builtin_bit_cast(float, wb << 16), __builtin_bit_cast(float, wb & 0xffff0000u)};
;                         const f32x2 af = {acc[ai][0][m][n][e], acc[ai][0][m][n][e + 1]}, ab = {acc[ai][1][m][n][e], acc[ai][1][m][n][e + 1]};
;                         const f32x2 nf = yf2 * cf + df, nb = yb2 * cb + db;
;                         const f32x2 xf = __builtin_elementwise_min(af * kr, (f32x2){60.f, 60.f}), xb = __builtin_elementwise_min(ab * kr, (f32x2){60.f, 60.f});
;                         const f32x2 pf = (f32x2){__builtin_amdgcn_exp2f(xf[0]), __builtin_amdgcn_exp2f(xf[1])} + 1.0f, pb = (f32x2){__builtin_amdgcn_exp2f(xb[0]), __builtin_amdgcn_exp2f(xb[1])} + 1.0f;
;                         const f32x2 den = pf * pb, num = (af * nf) * pb + (ab * nb) * pf;
;                         const f32x2 res = num * (f32x2){__builtin_amdgcn_rcpf(den[0]), __builtin_amdgcn_rcpf(den[1])};
;                         o[q] = res[0]; o[q + 1] = res[1]; }
;                 u32x4 w; w.x = cvt_pk_bf16(o[0], o[1]); w.y = cvt_pk_bf16(o[2], o[3]); w.z = cvt_pk_bf16(o[4], o[5]); w.w = cvt_pk_bf16(o[6], o[7]);
	v_mul_f32_e32 v22, v20, v22
	v_mul_f32_e32 v24, v20, v24
	v_mul_f32_e32 v20, 0xbfb8aa3b, v20
	v_pk_mul_f32 v[34:35], v[16:17], v[20:21] op_sel_hi:[1,0]
	v_mul_f32_e64 v26, v22, -v21
	v_min_f32_e32 v21, 0x42700000, v35
	v_mul_f32_e64 v28, v24, -v23
	v_pk_fma_f32 v[30:31], v[22:23], v[30:31], v[26:27] op_sel_hi:[0,1,0]
	v_min_f32_e32 v23, 0x42700000, v34
	v_pk_mul_f32 v[34:35], v[12:13], v[20:21] op_sel_hi:[1,0]
	v_pk_fma_f32 v[32:33], v[24:25], v[32:33], v[28:29] op_sel_hi:[0,1,0]
	v_min_f32_e32 v25, 0x42700000, v35
	v_min_f32_e32 v27, 0x42700000, v34
	v_exp_f32_e32 v34, v23
	v_exp_f32_e32 v35, v21
	v_exp_f32_e32 v36, v27
	v_exp_f32_e32 v37, v25
	v_pk_mul_f32 v[16:17], v[16:17], v[30:31]
	v_pk_add_f32 v[34:35], v[34:35], 1.0 op_sel_hi:[1,0]
	v_pk_mul_f32 v[12:13], v[12:13], v[32:33]
	v_pk_add_f32 v[36:37], v[36:37], 1.0 op_sel_hi:[1,0]
	v_pk_mul_f32 v[32:33], v[18:19], v[20:21] op_sel_hi:[1,0]
	v_pk_mul_f32 v[38:39], v[34:35], v[36:37]
	v_pk_mul_f32 v[16:17], v[16:17], v[36:37]
	v_min_f32_e32 v21, 0x42700000, v33
	v_pk_fma_f32 v[12:13], v[12:13], v[34:35], v[16:17]
	v_rcp_f32_e32 v16, v38
	v_rcp_f32_e32 v17, v39
	v_lshlrev_b32_e32 v30, 16, v69
	v_and_b32_e32 v31, 0xffff0000, v69
	v_pk_fma_f32 v[30:31], v[24:25], v[30:31], v[28:29] op_sel_hi:[0,1,0]
	v_pk_mul_f32 v[12:13], v[12:13], v[16:17]
	v_lshlrev_b32_e32 v16, 16, v73
	v_and_b32_e32 v17, 0xffff0000, v73
	v_pk_fma_f32 v[16:17], v[22:23], v[16:17], v[26:27] op_sel_hi:[0,1,0]
	v_min_f32_e32 v23, 0x42700000, v32
	v_pk_mul_f32 v[32:33], v[14:15], v[20:21] op_sel_hi:[1,0]
	v_pk_mul_f32 v[16:17], v[18:19], v[16:17]
	v_min_f32_e32 v25, 0x42700000, v33
	v_min_f32_e32 v27, 0x42700000, v32
	v_exp_f32_e32 v32, v23
	v_exp_f32_e32 v33, v21
	v_exp_f32_e32 v34, v27
	v_exp_f32_e32 v35, v25
	v_pk_mul_f32 v[14:15], v[14:15], v[30:31]
	v_pk_add_f32 v[32:33], v[32:33], 1.0 op_sel_hi:[1,0]
	v_pk_mul_f32 v[30:31], v[8:9], v[20:21] op_sel_hi:[1,0]
	v_pk_add_f32 v[34:35], v[34:35], 1.0 op_sel_hi:[1,0]
	v_min_f32_e32 v21, 0x42700000, v31
	v_pk_mul_f32 v[36:37], v[32:33], v[34:35]
	v_pk_mul_f32 v[16:17], v[16:17], v[34:35]
	v_lshlrev_b32_e32 v18, 16, v70
	v_pk_fma_f32 v[14:15], v[14:15], v[32:33], v[16:17]
	v_rcp_f32_e32 v16, v36
	v_rcp_f32_e32 v17, v37
	v_and_b32_e32 v19, 0xffff0000, v70
	v_pk_fma_f32 v[18:19], v[24:25], v[18:19], v[28:29] op_sel_hi:[0,1,0]
	v_pk_mul_f32 v[14:15], v[14:15], v[16:17]
	v_lshlrev_b32_e32 v16, 16, v74
	v_and_b32_e32 v17, 0xffff0000, v74
	v_pk_fma_f32 v[16:17], v[22:23], v[16:17], v[26:27] op_sel_hi:[0,1,0]
	v_min_f32_e32 v23, 0x42700000, v30
	v_pk_mul_f32 v[30:31], v[4:5], v[20:21] op_sel_hi:[1,0]
	v_pk_mul_f32 v[8:9], v[8:9], v[16:17]
	v_min_f32_e32 v25, 0x42700000, v31
	v_min_f32_e32 v27, 0x42700000, v30
	v_exp_f32_e32 v30, v23
	v_exp_f32_e32 v31, v21
	v_exp_f32_e32 v32, v27
	v_exp_f32_e32 v33, v25
	v_pk_mul_f32 v[4:5], v[4:5], v[18:19]
	v_pk_add_f32 v[30:31], v[30:31], 1.0 op_sel_hi:[1,0]
	v_pk_mul_f32 v[18:19], v[10:11], v[20:21] op_sel_hi:[1,0]
	v_pk_add_f32 v[32:33], v[32:33], 1.0 op_sel_hi:[1,0]
	v_min_f32_e32 v21, 0x42700000, v19
	v_pk_mul_f32 v[34:35], v[30:31], v[32:33]
	v_pk_mul_f32 v[8:9], v[8:9], v[32:33]
	v_lshlrev_b32_e32 v16, 16, v71
	v_pk_fma_f32 v[4:5], v[4:5], v[30:31], v[8:9]
	v_rcp_f32_e32 v8, v34
	v_rcp_f32_e32 v9, v35
	v_and_b32_e32 v17, 0xffff0000, v71
	v_pk_fma_f32 v[16:17], v[24:25], v[16:17], v[28:29] op_sel_hi:[0,1,0]
	v_pk_mul_f32 v[8:9], v[4:5], v[8:9]
	v_lshlrev_b32_e32 v4, 16, v75
	v_and_b32_e32 v5, 0xffff0000, v75
	v_pk_fma_f32 v[4:5], v[22:23], v[4:5], v[26:27] op_sel_hi:[0,1,0]
	v_min_f32_e32 v22, 0x42700000, v18
	v_pk_mul_f32 v[18:19], v[6:7], v[20:21] op_sel_hi:[1,0]
	v_pk_mul_f32 v[4:5], v[10:11], v[4:5]
	v_min_f32_e32 v23, 0x42700000, v19
	v_min_f32_e32 v20, 0x42700000, v18
	v_exp_f32_e32 v18, v22
	v_exp_f32_e32 v19, v21
	v_exp_f32_e32 v20, v20
	v_exp_f32_e32 v21, v23
	v_pk_mul_f32 v[6:7], v[6:7], v[16:17]
	v_pk_add_f32 v[18:19], v[18:19], 1.0 op_sel_hi:[1,0]
	v_pk_add_f32 v[20:21], v[20:21], 1.0 op_sel_hi:[1,0]
	s_nop 0
	v_pk_mul_f32 v[22:23], v[18:19], v[20:21]
	v_pk_mul_f32 v[4:5], v[4:5], v[20:21]
	s_nop 0
	v_pk_fma_f32 v[4:5], v[6:7], v[18:19], v[4:5]
	v_rcp_f32_e32 v6, v22
	v_rcp_f32_e32 v7, v23
	s_nop 0
	v_pk_mul_f32 v[10:11], v[4:5], v[6:7]
	v_cvt_pk_bf16_f32 v4, v12, v13
	v_cvt_pk_bf16_f32 v5, v14, v15
	v_cvt_pk_bf16_f32 v6, v8, v9
	v_lshl_add_u64 v[8:9], s[4:5], 0, v[112:113]
	v_lshl_add_u64 v[8:9], v[8:9], 0, v[188:189]
	v_cvt_pk_bf16_f32 v7, v10, v11
	global_store_dwordx4 v[8:9], v[4:7], off
	s_cbranch_vccnz .LBB0_335
	s_andn2_b64 vcc, exec, s[0:1]
	s_cbranch_vccnz .LBB0_334
	s_barrier
	s_branch .LBB0_334
